# RWKV scan helper waves: chunk operand loads ping-pong between the two register sets (loop body twice with the sets swapped), no register copies or vmcnt(0) drain at the latch; each body waits for its
# speedup vs baseline: 1.0074x; 1.0047x over previous
; __device__ __forceinline__ void scan_unit(Frame& F, const Args& a, int layer, int unit) {
;     ...
;         unsigned long long ph_act = 0ull;
;     ...
;         HELP_LOAD(cur, 0, -2);
;         for (int it = 0; it < NCH + 2; ++it) {
;     ...
;             const unsigned long long ph0 = __builtin_amdgcn_s_memtime();
;     ...
;             HELP_LOAD(nxt, it + 1, it - 1);
;     ...
;             cur = nxt;
;     ...
;             asm volatile("s_waitcnt vmcnt(0) lgkmcnt(0)" ::: "memory"); ph_act += __builtin_amdgcn_s_memtime() - ph0;
;     ...
;             __syncthreads();
;         }
.LBB0_1321:
	s_mov_b64 s[2:3], 0x30000
	s_add_i32 s0, s0, 1
	v_lshl_add_u64 v[44:45], v[44:45], 0, s[2:3]
	s_mov_b64 s[2:3], 0x10000
	v_lshl_add_u64 v[46:47], v[46:47], 0, s[2:3]
	s_cmpk_lg_i32 s0, 0x80
	s_waitcnt lgkmcnt(0)
	s_barrier
	s_cbranch_scc0 .LBB0_1335
	s_branch .Lhb_1322
.LBB0_1322:
	s_mov_b32 s100, 0
	s_mov_b32 s101, 0
	s_add_i32 s20, s0, 2
	s_cmpk_gt_u32 s20, 0x7e
	s_cbranch_scc1 .LBB0_1324
	v_lshl_add_u64 v[2:3], v[44:45], 0, v[42:43]
	v_add_co_u32_e32 v4, vcc, 0x1a430000, v2
	v_lshl_add_u64 v[8:9], v[46:47], 0, v[42:43]
	s_nop 0
	v_addc_co_u32_e32 v5, vcc, 0, v3, vcc
	v_add_co_u32_e32 v6, vcc, 0x1a431000, v2
	s_nop 1
	v_addc_co_u32_e32 v7, vcc, 0, v3, vcc
	v_add_co_u32_e32 v10, vcc, 0x38410000, v8
	global_load_dwordx2 v[52:53], v[4:5], off
	global_load_dwordx2 v[50:51], v[4:5], off offset:2048
	global_load_dwordx2 v[48:49], v[6:7], off
	global_load_dwordx2 v[54:55], v[6:7], off offset:2048
	v_addc_co_u32_e32 v11, vcc, 0, v9, vcc
	v_add_co_u32_e32 v12, vcc, 0x3c410000, v8
	s_nop 1
	v_addc_co_u32_e32 v13, vcc, 0, v9, vcc
	v_add_co_u32_e32 v4, vcc, 0x1a432000, v2
	global_load_dwordx2 v[58:59], v[10:11], off
	global_load_dwordx2 v[56:57], v[12:13], off
	global_load_dwordx2 v[60:61], v[12:13], off offset:2048
	global_load_dwordx2 v[62:63], v[10:11], off offset:2048
	v_addc_co_u32_e32 v5, vcc, 0, v3, vcc
	v_add_co_u32_e32 v6, vcc, 0x1a433000, v2
	s_nop 1
	v_addc_co_u32_e32 v7, vcc, 0, v3, vcc
	v_add_co_u32_e32 v10, vcc, 0x1a434000, v2
	s_nop 1
	v_addc_co_u32_e32 v11, vcc, 0, v3, vcc
	global_load_dwordx2 v[70:71], v[4:5], off
	global_load_dwordx2 v[68:69], v[4:5], off offset:2048
	global_load_dwordx2 v[64:65], v[6:7], off offset:2048
	global_load_dwordx2 v[66:67], v[10:11], off
	v_add_co_u32_e32 v4, vcc, 0x38411000, v8
	s_nop 1
	v_addc_co_u32_e32 v5, vcc, 0, v9, vcc
	v_add_co_u32_e32 v6, vcc, 0x3c411000, v8
	s_nop 1
	v_addc_co_u32_e32 v7, vcc, 0, v9, vcc
	v_add_co_u32_e32 v2, vcc, 0x1a435000, v2
	global_load_dwordx2 v[72:73], v[4:5], off
	global_load_dwordx2 v[74:75], v[6:7], off
	v_addc_co_u32_e32 v3, vcc, 0, v3, vcc
	global_load_dwordx2 v[76:77], v[2:3], off
	s_mov_b32 s100, 1

.LBB0_1328:
	v_mov_b64_e32 v[2:3], v[18:19]
	s_andn2_b64 vcc, exec, s[2:3]
	v_mov_b64_e32 v[4:5], v[20:21]
	s_cbranch_vccnz .LBB0_1331
	s_add_i32 s30, s0, 1
	s_lshl_b64 s[2:3], s[30:31], 16
	v_lshl_add_u64 v[2:3], v[30:31], 0, s[2:3]
	global_load_dwordx4 v[2:5], v[2:3], off
	s_mov_b32 s101, 1
	s_cmp_lt_u32 s20, 2
	s_cbranch_scc0 .LBB0_1332

; __device__ __forceinline__ void unpk8(const u32x4 w, f32x4& a, f32x4& b) { a = (f32x4){bflo(w.x), bfhi(w.x), bflo(w.y), bfhi(w.y)}; b = (f32x4){bflo(w.z), bfhi(w.z), bflo(w.w), bfhi(w.w)}; }
; #define LAS __attribute__((address_space(3)))
; __device__ __forceinline__ void scan_unit(Frame& F, const Args& a, int layer, int unit) {
;     ...
;             if (it >= 2) {
;                 const LAS float* buf = bufs + (it & 1) * SC_BUF; const LAS float* yb = sY + (it & 1) * SC_VEC;
;                 const size_t row = (size_t)b * SEQ + (size_t)(it - 2) * SC + tl; const int o = tl * 64 + c8 * 8;
;                 f32x4 y_[2], v_[2], g_[2];
; #pragma unroll
;                 for (int i = 0; i < 2; ++i) { y_[i] = *(const LAS f32x4*)(yb + o + 4 * i); v_[i] = *(const LAS f32x4*)(buf + SC_VP + o + 4 * i); }
;                 const float bon = buf[SC_BON + tl * 8 + c8];
;                 unpk8(cur.gt, g_[0], g_[1]);
.LBB0_1332:
	s_and_b32 s100, s100, s101
	s_cbranch_scc1 .Lhpa_w1
	s_waitcnt vmcnt(0)
	s_branch .Lhpa_g1

; #define UNP4(W) ((f32x4){bflo((W).x), bfhi((W).x), bflo((W).y), bfhi((W).y)})
; #define EXP4(E) ((f32x4){__builtin_amdgcn_exp2f(-1.44269504f * (E).x), __builtin_amdgcn_exp2f(-1.44269504f * (E).y), __builtin_amdgcn_exp2f(-1.44269504f * (E).z), __builtin_amdgcn_exp2f(-1.44269504f * (E).w)})
; #define SUM16(X) sum16_ns(X)
; __device__ __forceinline__ void scan_unit(Frame& F, const Args& a, int layer, int unit) {
;     ...
;                 const f32x4 pkk_ = *(const f32x4*)(a.in[11] + pop), pka_ = *(const f32x4*)(a.in[12] + pop), prk_ = *(const f32x4*)(a.in[13] + pop);
;                 const f32x4 zk0 = UNP4(cur.k0), zk1 = UNP4(cur.k1), zk2 = UNP4(cur.k2), zk3 = UNP4(cur.k3);
;                 f32x4 kn0 = zk0 * pkk_, kn1 = zk1 * pkk_, kn2 = zk2 * pkk_, kn3 = zk3 * pkk_;
;                 kn0 = kn0 * __builtin_amdgcn_rsqf(fmaxf(SUM16(DOT4(kn0, kn0)), 1e-24f)); kn1 = kn1 * __builtin_amdgcn_rsqf(fmaxf(SUM16(DOT4(kn1, kn1)), 1e-24f));
;                 kn2 = kn2 * __builtin_amdgcn_rsqf(fmaxf(SUM16(DOT4(kn2, kn2)), 1e-24f)); kn3 = kn3 * __builtin_amdgcn_rsqf(fmaxf(SUM16(DOT4(kn3, kn3)), 1e-24f));
;                 const f32x4 r0 = UNP4(cur.r0), r1 = UNP4(cur.r1), v0 = UNP4(cur.v0), v1 = UNP4(cur.v1), v2 = UNP4(cur.v2);
;                 const f32x4 ar0 = UNP4(cur.a0), ar1 = UNP4(cur.a1), ar2 = UNP4(cur.a2);
;                 const f32x4 e0 = UNP4(cur.e0), e1 = UNP4(cur.e1), e2 = UNP4(cur.e2);
;                 const f32x4 w0 = EXP4(e0), w1 = EXP4(e1), w2 = EXP4(e2);
.Lhpa_g2:
	s_nop 1
	v_mov_b64_e32 v[14:15], v[192:193]
	v_mov_b64_e32 v[16:17], v[194:195]
	v_mov_b64_e32 v[10:11], v[196:197]
	v_mov_b64_e32 v[12:13], v[198:199]
	v_mov_b64_e32 v[6:7], v[200:201]
	v_mov_b64_e32 v[8:9], v[202:203]
	v_lshlrev_b32_e32 v118, 16, v100
	v_and_b32_e32 v119, 0xffff0000, v100
	v_lshlrev_b32_e32 v120, 16, v101
	v_and_b32_e32 v121, 0xffff0000, v101
	v_lshlrev_b32_e32 v108, 16, v102
	v_and_b32_e32 v109, 0xffff0000, v102
	v_lshlrev_b32_e32 v116, 16, v103
	v_and_b32_e32 v117, 0xffff0000, v103
	v_lshlrev_b32_e32 v112, 16, v104
	v_and_b32_e32 v113, 0xffff0000, v104
	v_lshlrev_b32_e32 v114, 16, v105
	v_and_b32_e32 v115, 0xffff0000, v105
	v_lshlrev_b32_e32 v18, 16, v106
	v_and_b32_e32 v19, 0xffff0000, v106
	v_lshlrev_b32_e32 v20, 16, v107
	v_and_b32_e32 v21, 0xffff0000, v107
	v_and_b32_e32 v156, 0xffff0000, v98
	v_lshlrev_b32_e32 v158, 16, v99
	v_and_b32_e32 v160, 0xffff0000, v99
	v_lshlrev_b32_e32 v99, 16, v87
	v_and_b32_e32 v87, 0xffff0000, v87
	v_and_b32_e32 v149, 0xffff0000, v81
	s_bitcmp1_b32 s20, 0
	v_and_b32_e32 v151, 0xffff0000, v92
	v_lshlrev_b32_e32 v152, 16, v93
	v_and_b32_e32 v153, 0xffff0000, v93
	v_lshlrev_b32_e32 v150, 16, v92
	v_lshlrev_b32_e32 v92, 16, v90
	v_and_b32_e32 v93, 0xffff0000, v90
	v_lshlrev_b32_e32 v90, 16, v91
	v_and_b32_e32 v91, 0xffff0000, v91
	v_lshlrev_b32_e32 v154, 16, v96
	v_and_b32_e32 v155, 0xffff0000, v96
	v_lshlrev_b32_e32 v96, 16, v97
	v_and_b32_e32 v97, 0xffff0000, v97
	s_cselect_b32 s1, 0xb900, 0
	s_add_i32 s1, s1, 0
	v_mov_b32_e32 v157, v0
	v_mov_b32_e32 v159, v0
	v_mov_b32_e32 v161, v0
	v_pk_mul_f32 v[22:23], v[14:15], v[118:119]
	v_pk_mul_f32 v[24:25], v[16:17], v[120:121]
	v_pk_mul_f32 v[26:27], v[14:15], v[108:109]
	v_pk_mul_f32 v[28:29], v[16:17], v[116:117]
	v_pk_mul_f32 v[100:101], v[14:15], v[112:113]
	v_pk_mul_f32 v[102:103], v[16:17], v[114:115]
	v_pk_mul_f32 v[20:21], v[16:17], v[20:21]
	v_pk_mul_f32 v[18:19], v[14:15], v[18:19]
	v_pk_mul_f32 v[14:15], v[24:25], v[24:25]
	v_pk_mul_f32 v[16:17], v[22:23], v[22:23]
	v_pk_mul_f32 v[104:105], v[28:29], v[28:29]
	v_pk_mul_f32 v[106:107], v[26:27], v[26:27]
	v_pk_mov_b32 v[146:147], v[16:17], v[14:15] op_sel:[1,0]
	v_mov_b32_e32 v17, v15
	v_pk_mov_b32 v[14:15], v[106:107], v[104:105] op_sel:[1,0]
	v_mov_b32_e32 v107, v105
	v_pk_mul_f32 v[110:111], v[102:103], v[102:103]
	v_pk_mul_f32 v[122:123], v[100:101], v[100:101]
	v_pk_add_f32 v[16:17], v[146:147], v[16:17]
	v_pk_add_f32 v[14:15], v[14:15], v[106:107]
	v_pk_mov_b32 v[104:105], v[122:123], v[110:111] op_sel:[1,0]
	v_mov_b32_e32 v123, v111
	v_add_f32_e32 v16, v16, v17
	v_add_f32_e32 v14, v14, v15
	v_mul_f32_e32 v145, v19, v19
	v_mul_f32_e32 v148, v21, v21
	v_pk_add_f32 v[104:105], v[104:105], v[122:123]
	v_add_f32_dpp v16, v16, v16 quad_perm:[1,0,3,2] row_mask:0xf bank_mask:0xf bound_ctrl:1
	v_add_f32_dpp v14, v14, v14 quad_perm:[1,0,3,2] row_mask:0xf bank_mask:0xf bound_ctrl:1
	v_fmac_f32_e32 v145, v18, v18
	v_fmac_f32_e32 v148, v20, v20
	v_add_f32_e32 v15, v104, v105
	v_add_f32_e32 v106, v145, v148
	v_lshlrev_b32_e32 v122, 16, v98
	v_add_f32_dpp v15, v15, v15 quad_perm:[1,0,3,2] row_mask:0xf bank_mask:0xf bound_ctrl:1
	v_add_f32_dpp v16, v16, v16 quad_perm:[2,3,0,1] row_mask:0xf bank_mask:0xf bound_ctrl:1
	v_add_f32_dpp v14, v14, v14 quad_perm:[2,3,0,1] row_mask:0xf bank_mask:0xf bound_ctrl:1
	v_add_f32_dpp v17, v106, v106 quad_perm:[1,0,3,2] row_mask:0xf bank_mask:0xf bound_ctrl:1
	v_lshlrev_b32_e32 v98, 16, v86
	v_and_b32_e32 v86, 0xffff0000, v86
	v_add_f32_dpp v15, v15, v15 quad_perm:[2,3,0,1] row_mask:0xf bank_mask:0xf bound_ctrl:1
	v_add_f32_dpp v16, v16, v16 row_half_mirror row_mask:0xf bank_mask:0xf bound_ctrl:1
	v_add_f32_dpp v14, v14, v14 row_half_mirror row_mask:0xf bank_mask:0xf bound_ctrl:1
	v_add_f32_dpp v17, v17, v17 quad_perm:[2,3,0,1] row_mask:0xf bank_mask:0xf bound_ctrl:1
	v_lshlrev_b32_e32 v110, 16, v95
	v_and_b32_e32 v95, 0xffff0000, v95
	v_add_f32_dpp v15, v15, v15 row_half_mirror row_mask:0xf bank_mask:0xf bound_ctrl:1
	v_add_f32_dpp v16, v16, v16 row_mirror row_mask:0xf bank_mask:0xf bound_ctrl:1
	v_add_f32_dpp v14, v14, v14 row_mirror row_mask:0xf bank_mask:0xf bound_ctrl:1
	v_add_f32_dpp v17, v17, v17 row_half_mirror row_mask:0xf bank_mask:0xf bound_ctrl:1
	v_lshlrev_b32_e32 v146, 16, v80
	v_max_f32_e32 v16, v16, v16
	v_add_f32_dpp v15, v15, v15 row_mirror row_mask:0xf bank_mask:0xf bound_ctrl:1
	v_max_f32_e32 v14, v14, v14
	v_add_f32_dpp v107, v17, v17 row_mirror row_mask:0xf bank_mask:0xf bound_ctrl:1
	v_max_f32_e32 v16, 0x179abe15, v16
	v_max_f32_e32 v17, 0x179abe15, v14
	v_max_f32_e32 v15, v15, v15
	v_rsq_f32_e32 v14, v16
	v_rsq_f32_e32 v16, v17
	v_max_f32_e32 v15, 0x179abe15, v15
	v_rsq_f32_e32 v106, v15
	v_pk_mul_f32 v[104:105], v[26:27], v[16:17] op_sel_hi:[1,0]
	v_pk_mul_f32 v[26:27], v[28:29], v[16:17] op_sel_hi:[1,0]
	v_max_f32_e32 v28, v107, v107
	v_max_f32_e32 v28, 0x179abe15, v28
	v_pk_mul_f32 v[24:25], v[24:25], v[14:15] op_sel_hi:[1,0]
	v_pk_mul_f32 v[22:23], v[22:23], v[14:15] op_sel_hi:[1,0]
	v_pk_mul_f32 v[16:17], v[100:101], v[106:107] op_sel_hi:[1,0]
	v_pk_mul_f32 v[14:15], v[102:103], v[106:107] op_sel_hi:[1,0]
	v_rsq_f32_e32 v106, v28
	v_lshlrev_b32_e32 v28, 16, v88
	v_and_b32_e32 v29, 0xffff0000, v88
	v_lshlrev_b32_e32 v88, 16, v78
	v_and_b32_e32 v78, 0xffff0000, v78
	v_lshlrev_b32_e32 v100, 16, v82
	v_and_b32_e32 v101, 0xffff0000, v82
	v_lshlrev_b32_e32 v102, 16, v83
	v_and_b32_e32 v103, 0xffff0000, v83
	v_lshlrev_b32_e32 v82, 16, v89
	v_and_b32_e32 v83, 0xffff0000, v89
	v_lshlrev_b32_e32 v89, 16, v79
	v_mul_f32_e32 v78, 0xbfb8aa3b, v78
	v_and_b32_e32 v79, 0xffff0000, v79
	v_exp_f32_e32 v163, v78
	v_mul_f32_e32 v78, 0xbfb8aa3b, v89
; #define LAS __attribute__((address_space(3)))
; #define SUM16(X) sum16_ns(X)
; __device__ __forceinline__ void scan_unit(Frame& F, const Args& a, int layer, int unit) {
;     ...
;                 const f32x4 w0 = EXP4(e0), w1 = EXP4(e1), w2 = EXP4(e2);
;                 const f32x4 a1v = -kn1, a2v = -kn2, a3v = -kn3;
;                 const f32x4 b0 = kn0 * ar0, b1 = kn1 * ar1, b2 = kn2 * ar2;
;                 const f32x4 kp0 = zk0 * (1.f + (ar0 - 1.f) * pka_), kp1 = zk1 * (1.f + (ar1 - 1.f) * pka_), kp2 = zk2 * (1.f + (ar2 - 1.f) * pka_);
;                 const f32x4 W2 = w0 * w1, Bt = b0 * w1, Kt = kp0 * w1, x0v = a2v, x1v = w2 * a3v;
;                 const f32x4 X0 = W2 * x0v, X1 = W2 * x1v, X2 = w0 * r0, X3 = W2 * r1;
;                 *(LAS f32x4*)(buf + SC_WW + pr * 64 + c4 * 4) = W2;
;                 *(LAS f32x4*)(buf + SC_VP + (2 * pr) * 64 + c4 * 4) = v0; *(LAS f32x4*)(buf + SC_VP + (2 * pr + 1) * 64 + c4 * 4) = v1;
;                 { LAS f32x4* vq = (LAS f32x4*)(buf + SC_VQ + pr * 256 + c4 * 16);
;                   vq[0] = (f32x4){v0.x, v1.x, v2.x, 0.f}; vq[1] = (f32x4){v0.y, v1.y, v2.y, 0.f}; vq[2] = (f32x4){v0.z, v1.z, v2.z, 0.f}; vq[3] = (f32x4){v0.w, v1.w, v2.w, 0.f}; }
;                 { LAS v2u* bkp = (LAS v2u*)(buf + SC_BK + pr * 128) + (((c4 & 3) * 4) * 4 + (c4 >> 2));
;                   bkp[0] = (v2u){cvt_pk_bf16(Bt.x, Kt.x), cvt_pk_bf16(b1.x, kp1.x)}; bkp[4] = (v2u){cvt_pk_bf16(Bt.y, Kt.y), cvt_pk_bf16(b1.y, kp1.y)};
;                   bkp[8] = (v2u){cvt_pk_bf16(Bt.z, Kt.z), cvt_pk_bf16(b1.z, kp1.z)}; bkp[12] = (v2u){cvt_pk_bf16(Bt.w, Kt.w), cvt_pk_bf16(b1.w, kp1.w)}; }
;                 { LAS unsigned char* xp = (LAS unsigned char*)(buf + SC_XA) + pr * 512 + (c4 >> 3) * 64 + (c4 & 3) * 16 + ((c4 >> 2) & 1) * 8;
;                   *(LAS v2u*)xp = (v2u){cvt_pk_bf16(X0.x, X0.y), cvt_pk_bf16(X0.z, X0.w)}; *(LAS v2u*)(xp + 128) = (v2u){cvt_pk_bf16(X1.x, X1.y), cvt_pk_bf16(X1.z, X1.w)};
;                   *(LAS v2u*)(xp + 256) = (v2u){cvt_pk_bf16(X2.x, X2.y), cvt_pk_bf16(X2.z, X2.w)}; *(LAS v2u*)(xp + 384) = (v2u){cvt_pk_bf16(X3.x, X3.y), cvt_pk_bf16(X3.z, X3.w)}; }
;                 const f32x4 ca = (f32x4){SUM16(DOT4(Bt, x0v)), SUM16(DOT4(Kt, x0v)), SUM16(DOT4(b1, x0v)), SUM16(DOT4(kp1, x0v))};
;                 const f32x4 cb = (f32x4){SUM16(DOT4(Bt, x1v)), SUM16(DOT4(Kt, x1v)), SUM16(DOT4(b1, x1v)), SUM16(DOT4(kp1, x1v))};
	v_exp_f32_e32 v164, v78
	v_mul_f32_e32 v78, 0xbfb8aa3b, v79
	v_exp_f32_e32 v165, v78
	v_mul_f32_e32 v78, 0xbfb8aa3b, v98
	v_exp_f32_e32 v166, v78
	v_mul_f32_e32 v78, 0xbfb8aa3b, v86
	v_exp_f32_e32 v167, v78
	v_mul_f32_e32 v78, 0xbfb8aa3b, v99
	v_lshlrev_b32_e32 v107, 16, v94
	v_exp_f32_e32 v168, v78
	v_mul_f32_e32 v78, 0xbfb8aa3b, v87
	v_and_b32_e32 v94, 0xffff0000, v94
	v_exp_f32_e32 v169, v78
	v_mul_f32_e32 v78, 0xbfb8aa3b, v107
	v_exp_f32_e32 v170, v78
	v_mul_f32_e32 v78, 0xbfb8aa3b, v94
	v_exp_f32_e32 v171, v78
	v_mul_f32_e32 v78, 0xbfb8aa3b, v110
	v_and_b32_e32 v147, 0xffff0000, v80
	v_lshlrev_b32_e32 v148, 16, v81
	v_lshlrev_b32_e32 v80, 16, v84
	v_and_b32_e32 v81, 0xffff0000, v84
	v_mul_f32_e32 v88, 0xbfb8aa3b, v88
	v_exp_f32_e32 v172, v78
	v_mul_f32_e32 v78, 0xbfb8aa3b, v95
	v_lshlrev_b32_e32 v84, 16, v85
	v_and_b32_e32 v85, 0xffff0000, v85
	v_exp_f32_e32 v162, v88
	v_exp_f32_e32 v173, v78
	v_pk_add_f32 v[78:79], v[80:81], -1.0 op_sel_hi:[1,0]
	v_pk_mul_f32 v[98:99], v[20:21], v[106:107] op_sel_hi:[1,0] neg_lo:[0,1] neg_hi:[0,1]
	v_pk_mul_f32 v[20:21], v[22:23], v[80:81]
	v_pk_add_f32 v[80:81], v[84:85], -1.0 op_sel_hi:[1,0]
	v_pk_fma_f32 v[78:79], v[78:79], v[10:11], 1.0 op_sel_hi:[1,1,0]
	v_pk_mul_f32 v[22:23], v[24:25], v[84:85]
	v_pk_mul_f32 v[24:25], v[26:27], v[90:91]
	v_pk_mul_f32 v[88:89], v[104:105], v[92:93]
	v_pk_fma_f32 v[84:85], v[80:81], v[12:13], 1.0 op_sel_hi:[1,1,0]
	v_pk_mul_f32 v[80:81], v[78:79], v[118:119]
	v_pk_add_f32 v[78:79], v[90:91], -1.0 op_sel_hi:[1,0]
	v_pk_add_f32 v[86:87], v[92:93], -1.0 op_sel_hi:[1,0]
	v_pk_add_f32 v[90:91], v[96:97], -1.0 op_sel_hi:[1,0]
	v_pk_add_f32 v[92:93], v[154:155], -1.0 op_sel_hi:[1,0]
	v_pk_mul_f32 v[84:85], v[84:85], v[120:121]
	v_pk_fma_f32 v[86:87], v[86:87], v[10:11], 1.0 op_sel_hi:[1,1,0]
	v_pk_fma_f32 v[78:79], v[78:79], v[12:13], 1.0 op_sel_hi:[1,1,0]
	v_pk_fma_f32 v[10:11], v[92:93], v[10:11], 1.0 op_sel_hi:[1,1,0]
	v_pk_fma_f32 v[12:13], v[90:91], v[12:13], 1.0 op_sel_hi:[1,1,0]
	v_lshlrev_b32_e32 v120, 2, v127
	v_pk_mul_f32 v[106:107], v[18:19], v[106:107] op_sel_hi:[1,0] neg_lo:[0,1] neg_hi:[0,1]
	v_pk_mul_f32 v[78:79], v[78:79], v[116:117]
	v_pk_mul_f32 v[86:87], v[86:87], v[108:109]
	v_pk_mul_f32 v[108:109], v[12:13], v[114:115]
	v_pk_mul_f32 v[112:113], v[10:11], v[112:113]
	v_pk_mul_f32 v[12:13], v[168:169], v[164:165]
	v_pk_mul_f32 v[10:11], v[166:167], v[162:163]
	v_pk_mul_f32 v[116:117], v[172:173], v[98:99]
	v_add3_u32 v121, s1, v130, v120
	v_pk_mul_f32 v[94:95], v[168:169], v[22:23]
	v_pk_mul_f32 v[90:91], v[168:169], v[84:85]
	v_pk_mul_f32 v[114:115], v[170:171], v[106:107]
	v_pk_mul_f32 v[118:119], v[12:13], v[14:15] neg_lo:[0,1] neg_hi:[0,1]
	v_pk_mul_f32 v[168:169], v[12:13], v[116:117]
	v_pk_mul_f32 v[172:173], v[82:83], v[12:13]
	ds_write_b128 v121, v[10:13]
	v_add_u32_e32 v12, s1, v131
	v_pk_mul_f32 v[18:19], v[14:15], v[96:97]
	v_pk_mul_f32 v[96:97], v[166:167], v[20:21]
	v_pk_mul_f32 v[92:93], v[166:167], v[80:81]
	v_pk_mul_f32 v[166:167], v[10:11], v[16:17] neg_lo:[0,1] neg_hi:[0,1]
	v_pk_mul_f32 v[170:171], v[10:11], v[114:115]
	v_pk_mul_f32 v[174:175], v[28:29], v[10:11]
	v_add_u32_e32 v10, v12, v120
	ds_write_b128 v10, v[146:149] offset:38144
	v_add3_u32 v10, s1, v132, v120
	v_pk_mul_f32 v[110:111], v[16:17], v[154:155]
	ds_write_b128 v10, v[150:153] offset:38144
	v_add3_u32 v10, s1, v133, v134
	v_mov_b32_e32 v154, v147
	v_mov_b32_e32 v155, v151
	ds_write_b128 v10, v[154:157] offset:4112
	v_mov_b32_e32 v156, v148
	v_mov_b32_e32 v157, v152
	v_mov_b32_e32 v120, v146
	v_mov_b32_e32 v121, v150
	v_mov_b32_e32 v123, v0
	ds_write_b128 v10, v[156:159] offset:4128
	v_mov_b32_e32 v158, v149
	v_mov_b32_e32 v159, v153
	ds_write_b128 v10, v[120:123] offset:4096
	ds_write_b128 v10, v[158:161] offset:4144
	v_add3_u32 v13, v12, v135, v142
	v_cvt_pk_bf16_f32 v10, v96, v92
	v_cvt_pk_bf16_f32 v11, v88, v86
	ds_write_b64 v13, v[10:11] offset:20480
	v_cvt_pk_bf16_f32 v10, v97, v93
	v_cvt_pk_bf16_f32 v11, v89, v87
	ds_write_b64 v13, v[10:11] offset:20512
	v_cvt_pk_bf16_f32 v10, v94, v90
	v_cvt_pk_bf16_f32 v11, v24, v78
	ds_write_b64 v13, v[10:11] offset:20544
	v_cvt_pk_bf16_f32 v10, v95, v91
	v_cvt_pk_bf16_f32 v11, v25, v79
	ds_write_b64 v13, v[10:11] offset:20576
	v_add_u32_e32 v10, v12, v136
	v_add3_u32 v12, v10, v137, v138
	v_cvt_pk_bf16_f32 v10, v166, v167
	v_cvt_pk_bf16_f32 v11, v118, v119
	ds_write_b64 v12, v[10:11] offset:28672
	v_cvt_pk_bf16_f32 v10, v170, v171
	v_cvt_pk_bf16_f32 v11, v168, v169
	v_pk_mul_f32 v[164:165], v[164:165], v[102:103]
	v_pk_mul_f32 v[162:163], v[162:163], v[100:101]
	ds_write_b64 v12, v[10:11] offset:28800
	v_cvt_pk_bf16_f32 v10, v162, v163
	v_cvt_pk_bf16_f32 v11, v164, v165
	ds_write_b64 v12, v[10:11] offset:28928
	v_cvt_pk_bf16_f32 v10, v174, v175
	v_cvt_pk_bf16_f32 v11, v172, v173
	ds_write_b64 v12, v[10:11] offset:29056
	v_mul_f32_e64 v10, v97, -v17
	v_mul_f32_e64 v11, v95, -v15
	v_fma_f32 v10, v96, -v16, v10
	v_fma_f32 v11, v94, -v14, v11
	v_add_f32_e32 v10, v10, v11
	v_mul_f32_e64 v11, v93, -v17
	v_mul_f32_e64 v12, v91, -v15
	v_fma_f32 v11, v92, -v16, v11
	v_fma_f32 v12, v90, -v14, v12
	v_add_f32_e32 v11, v11, v12
	v_mul_f32_e64 v12, v89, -v17
	v_mul_f32_e64 v13, v25, -v15
	v_fma_f32 v12, v88, -v16, v12
	v_fma_f32 v13, v24, -v14, v13
	v_add_f32_e32 v12, v12, v13
	v_mul_f32_e64 v13, v87, -v17
	v_mul_f32_e64 v15, v79, -v15
	v_fma_f32 v13, v86, -v16, v13
	v_fma_f32 v14, v78, -v14, v15
	v_add_f32_e32 v13, v13, v14
	v_mul_f32_e32 v14, v97, v115
	v_mul_f32_e32 v15, v95, v117
	v_fmac_f32_e32 v14, v96, v114
	v_fmac_f32_e32 v15, v94, v116
	v_add_f32_e32 v14, v14, v15
	v_mul_f32_e32 v15, v93, v115
	v_mul_f32_e32 v16, v91, v117
; #define SUM16(X) sum16_ns(X)
; __device__ __forceinline__ void scan_unit(Frame& F, const Args& a, int layer, int unit) {
;     ...
;                 const f32x4 ca = (f32x4){SUM16(DOT4(Bt, x0v)), SUM16(DOT4(Kt, x0v)), SUM16(DOT4(b1, x0v)), SUM16(DOT4(kp1, x0v))};
;                 const f32x4 cb = (f32x4){SUM16(DOT4(Bt, x1v)), SUM16(DOT4(Kt, x1v)), SUM16(DOT4(b1, x1v)), SUM16(DOT4(kp1, x1v))};
;                 const f32x4 cc = (f32x4){SUM16(DOT4(b2, a3v)), SUM16(DOT4(kp2, a3v)), SUM16(DOT4(b0, r0)), SUM16(DOT4(kp0, r0))};
;                 const f32x4 cd = (f32x4){SUM16(DOT4(Bt, r1)), SUM16(DOT4(Kt, r1)), SUM16(DOT4(b1, r1)), SUM16(DOT4(kp1, r1))};
;                 const float ci = SUM16(DOT4(kp0, a1v));
;                 const f32x4 z0 = r0 * kp0 * prk_, z1 = r1 * kp1 * prk_;
;                 const float bon0 = SUM16((z0.x + z0.y) + (z0.z + z0.w)), bon1 = SUM16((z1.x + z1.y) + (z1.z + z1.w));
	v_mul_f32_e32 v21, v21, v101
	v_fmac_f32_e32 v15, v92, v114
	v_fmac_f32_e32 v16, v90, v116
	v_fmac_f32_e32 v21, v20, v100
	v_mul_f32_e32 v20, v23, v103
	v_add_f32_e32 v15, v15, v16
	v_mul_f32_e32 v16, v89, v115
	v_mul_f32_e32 v17, v25, v117
	v_fmac_f32_e32 v20, v22, v102
	v_mul_f32_e32 v89, v89, v29
	v_mul_f32_e32 v25, v25, v83
	v_add_f32_e32 v20, v21, v20
	v_mul_f32_e32 v21, v81, v101
	v_mul_f32_e32 v22, v85, v103
	v_fmac_f32_e32 v89, v88, v28
	v_fmac_f32_e32 v25, v24, v82
	v_fmac_f32_e32 v16, v88, v114
	v_fmac_f32_e32 v17, v24, v116
	v_fmac_f32_e32 v21, v80, v100
	v_fmac_f32_e32 v22, v84, v102
	v_add_f32_e32 v24, v89, v25
	v_mul_f32_e32 v25, v87, v29
	v_mul_f32_e32 v88, v79, v83
	v_add_f32_e32 v21, v21, v22
	v_mul_f32_e32 v22, v97, v29
	v_mul_f32_e32 v23, v95, v83
	v_fmac_f32_e32 v25, v86, v28
	v_fmac_f32_e32 v88, v78, v82
	v_add_f32_e32 v16, v16, v17
	v_mul_f32_e32 v17, v87, v115
	v_fmac_f32_e32 v22, v96, v28
	v_fmac_f32_e32 v23, v94, v82
	v_add_f32_e32 v25, v25, v88
	v_mul_f32_e64 v88, v81, -v105
	v_mul_f32_e64 v27, v85, -v27
	v_fmac_f32_e32 v17, v86, v114
	v_mul_f32_e32 v114, v79, v117
	v_mul_f32_e32 v111, v111, v107
	v_mul_f32_e32 v19, v19, v99
	v_add_f32_e32 v22, v22, v23
	v_mul_f32_e32 v23, v93, v29
	v_fma_f32 v88, v80, -v104, v88
	v_fma_f32 v26, v84, -v26, v27
	v_pk_mul_f32 v[80:81], v[100:101], v[80:81]
	v_pk_mul_f32 v[84:85], v[102:103], v[84:85]
	v_fmac_f32_e32 v114, v78, v116
	v_fmac_f32_e32 v111, v110, v106
	v_fmac_f32_e32 v19, v18, v98
	v_fmac_f32_e32 v23, v92, v28
	v_pk_mul_f32 v[84:85], v[8:9], v[84:85]
	v_pk_mul_f32 v[80:81], v[6:7], v[80:81]
	v_pk_mul_f32 v[28:29], v[28:29], v[86:87]
	v_pk_mul_f32 v[78:79], v[82:83], v[78:79]
	v_add_f32_e32 v18, v111, v19
	v_mul_f32_e32 v19, v113, v107
	v_mul_f32_e32 v99, v109, v99
	v_mul_f32_e32 v91, v91, v83
	v_pk_mul_f32 v[8:9], v[8:9], v[78:79]
	v_pk_mul_f32 v[28:29], v[6:7], v[28:29]
	v_add_f32_e32 v6, v80, v81
	v_add_f32_e32 v7, v84, v85
	v_fmac_f32_e32 v19, v112, v106
	v_fmac_f32_e32 v99, v108, v98
	v_fmac_f32_e32 v91, v90, v82
	v_add_f32_e32 v6, v6, v7
	v_add_f32_e32 v7, v28, v29
	v_add_f32_e32 v8, v8, v9
	v_add_f32_e32 v17, v17, v114
	v_add_f32_e32 v19, v19, v99
	v_add_f32_e32 v23, v23, v91
	v_add_f32_e32 v26, v88, v26
	v_add_f32_e32 v7, v7, v8
	v_add_f32_dpp v10, v10, v10 quad_perm:[1,0,3,2] row_mask:0xf bank_mask:0xf bound_ctrl:1
	v_add_f32_dpp v11, v11, v11 quad_perm:[1,0,3,2] row_mask:0xf bank_mask:0xf bound_ctrl:1
	v_add_f32_dpp v12, v12, v12 quad_perm:[1,0,3,2] row_mask:0xf bank_mask:0xf bound_ctrl:1
	v_add_f32_dpp v13, v13, v13 quad_perm:[1,0,3,2] row_mask:0xf bank_mask:0xf bound_ctrl:1
	v_add_f32_dpp v14, v14, v14 quad_perm:[1,0,3,2] row_mask:0xf bank_mask:0xf bound_ctrl:1
	v_add_f32_dpp v15, v15, v15 quad_perm:[1,0,3,2] row_mask:0xf bank_mask:0xf bound_ctrl:1
	v_add_f32_dpp v16, v16, v16 quad_perm:[1,0,3,2] row_mask:0xf bank_mask:0xf bound_ctrl:1
	v_add_f32_dpp v17, v17, v17 quad_perm:[1,0,3,2] row_mask:0xf bank_mask:0xf bound_ctrl:1
	v_add_f32_dpp v18, v18, v18 quad_perm:[1,0,3,2] row_mask:0xf bank_mask:0xf bound_ctrl:1
	v_add_f32_dpp v19, v19, v19 quad_perm:[1,0,3,2] row_mask:0xf bank_mask:0xf bound_ctrl:1
	v_add_f32_dpp v20, v20, v20 quad_perm:[1,0,3,2] row_mask:0xf bank_mask:0xf bound_ctrl:1
	v_add_f32_dpp v21, v21, v21 quad_perm:[1,0,3,2] row_mask:0xf bank_mask:0xf bound_ctrl:1
	v_add_f32_dpp v22, v22, v22 quad_perm:[1,0,3,2] row_mask:0xf bank_mask:0xf bound_ctrl:1
	v_add_f32_dpp v23, v23, v23 quad_perm:[1,0,3,2] row_mask:0xf bank_mask:0xf bound_ctrl:1
	v_add_f32_dpp v24, v24, v24 quad_perm:[1,0,3,2] row_mask:0xf bank_mask:0xf bound_ctrl:1
	v_add_f32_dpp v25, v25, v25 quad_perm:[1,0,3,2] row_mask:0xf bank_mask:0xf bound_ctrl:1
	v_add_f32_dpp v26, v26, v26 quad_perm:[1,0,3,2] row_mask:0xf bank_mask:0xf bound_ctrl:1
	v_add_f32_dpp v6, v6, v6 quad_perm:[1,0,3,2] row_mask:0xf bank_mask:0xf bound_ctrl:1
	v_add_f32_dpp v7, v7, v7 quad_perm:[1,0,3,2] row_mask:0xf bank_mask:0xf bound_ctrl:1
	s_nop 1
	v_add_f32_dpp v10, v10, v10 quad_perm:[2,3,0,1] row_mask:0xf bank_mask:0xf bound_ctrl:1
	v_add_f32_dpp v11, v11, v11 quad_perm:[2,3,0,1] row_mask:0xf bank_mask:0xf bound_ctrl:1
	v_add_f32_dpp v12, v12, v12 quad_perm:[2,3,0,1] row_mask:0xf bank_mask:0xf bound_ctrl:1
	v_add_f32_dpp v13, v13, v13 quad_perm:[2,3,0,1] row_mask:0xf bank_mask:0xf bound_ctrl:1
	v_add_f32_dpp v14, v14, v14 quad_perm:[2,3,0,1] row_mask:0xf bank_mask:0xf bound_ctrl:1
	v_add_f32_dpp v15, v15, v15 quad_perm:[2,3,0,1] row_mask:0xf bank_mask:0xf bound_ctrl:1
	v_add_f32_dpp v16, v16, v16 quad_perm:[2,3,0,1] row_mask:0xf bank_mask:0xf bound_ctrl:1
	v_add_f32_dpp v17, v17, v17 quad_perm:[2,3,0,1] row_mask:0xf bank_mask:0xf bound_ctrl:1
; #define LAS __attribute__((address_space(3)))
; #define SUM16(X) sum16_ns(X)
; __device__ __forceinline__ void scan_unit(Frame& F, const Args& a, int layer, int unit) {
;     ...
;                 const f32x4 ca = (f32x4){SUM16(DOT4(Bt, x0v)), SUM16(DOT4(Kt, x0v)), SUM16(DOT4(b1, x0v)), SUM16(DOT4(kp1, x0v))};
;                 const f32x4 cb = (f32x4){SUM16(DOT4(Bt, x1v)), SUM16(DOT4(Kt, x1v)), SUM16(DOT4(b1, x1v)), SUM16(DOT4(kp1, x1v))};
;                 const f32x4 cc = (f32x4){SUM16(DOT4(b2, a3v)), SUM16(DOT4(kp2, a3v)), SUM16(DOT4(b0, r0)), SUM16(DOT4(kp0, r0))};
;                 const f32x4 cd = (f32x4){SUM16(DOT4(Bt, r1)), SUM16(DOT4(Kt, r1)), SUM16(DOT4(b1, r1)), SUM16(DOT4(kp1, r1))};
;                 const float ci = SUM16(DOT4(kp0, a1v));
;                 const f32x4 z0 = r0 * kp0 * prk_, z1 = r1 * kp1 * prk_;
;                 const float bon0 = SUM16((z0.x + z0.y) + (z0.z + z0.w)), bon1 = SUM16((z1.x + z1.y) + (z1.z + z1.w));
;                 if (c4 == 0) { LAS f32x4* cp = (LAS f32x4*)(buf + SC_C + pr * 20); cp[0] = ca; cp[1] = cb; cp[2] = cc; cp[3] = cd; cp[4] = (f32x4){ci, 0.f, 0.f, 0.f}; }
;                 buf[SC_BON + (2 * pr) * 8 + (c4 >> 1)] = bon0; buf[SC_BON + (2 * pr + 1) * 8 + (c4 >> 1)] = bon1;
	v_add_f32_dpp v18, v18, v18 quad_perm:[2,3,0,1] row_mask:0xf bank_mask:0xf bound_ctrl:1
	v_add_f32_dpp v19, v19, v19 quad_perm:[2,3,0,1] row_mask:0xf bank_mask:0xf bound_ctrl:1
	v_add_f32_dpp v20, v20, v20 quad_perm:[2,3,0,1] row_mask:0xf bank_mask:0xf bound_ctrl:1
	v_add_f32_dpp v21, v21, v21 quad_perm:[2,3,0,1] row_mask:0xf bank_mask:0xf bound_ctrl:1
	v_add_f32_dpp v22, v22, v22 quad_perm:[2,3,0,1] row_mask:0xf bank_mask:0xf bound_ctrl:1
	v_add_f32_dpp v23, v23, v23 quad_perm:[2,3,0,1] row_mask:0xf bank_mask:0xf bound_ctrl:1
	v_add_f32_dpp v24, v24, v24 quad_perm:[2,3,0,1] row_mask:0xf bank_mask:0xf bound_ctrl:1
	v_add_f32_dpp v25, v25, v25 quad_perm:[2,3,0,1] row_mask:0xf bank_mask:0xf bound_ctrl:1
	v_add_f32_dpp v26, v26, v26 quad_perm:[2,3,0,1] row_mask:0xf bank_mask:0xf bound_ctrl:1
	v_add_f32_dpp v6, v6, v6 quad_perm:[2,3,0,1] row_mask:0xf bank_mask:0xf bound_ctrl:1
	v_add_f32_dpp v7, v7, v7 quad_perm:[2,3,0,1] row_mask:0xf bank_mask:0xf bound_ctrl:1
	s_nop 1
	v_add_f32_dpp v10, v10, v10 row_half_mirror row_mask:0xf bank_mask:0xf bound_ctrl:1
	v_add_f32_dpp v11, v11, v11 row_half_mirror row_mask:0xf bank_mask:0xf bound_ctrl:1
	v_add_f32_dpp v12, v12, v12 row_half_mirror row_mask:0xf bank_mask:0xf bound_ctrl:1
	v_add_f32_dpp v13, v13, v13 row_half_mirror row_mask:0xf bank_mask:0xf bound_ctrl:1
	v_add_f32_dpp v14, v14, v14 row_half_mirror row_mask:0xf bank_mask:0xf bound_ctrl:1
	v_add_f32_dpp v15, v15, v15 row_half_mirror row_mask:0xf bank_mask:0xf bound_ctrl:1
	v_add_f32_dpp v16, v16, v16 row_half_mirror row_mask:0xf bank_mask:0xf bound_ctrl:1
	v_add_f32_dpp v17, v17, v17 row_half_mirror row_mask:0xf bank_mask:0xf bound_ctrl:1
	v_add_f32_dpp v18, v18, v18 row_half_mirror row_mask:0xf bank_mask:0xf bound_ctrl:1
	v_add_f32_dpp v19, v19, v19 row_half_mirror row_mask:0xf bank_mask:0xf bound_ctrl:1
	v_add_f32_dpp v20, v20, v20 row_half_mirror row_mask:0xf bank_mask:0xf bound_ctrl:1
	v_add_f32_dpp v21, v21, v21 row_half_mirror row_mask:0xf bank_mask:0xf bound_ctrl:1
	v_add_f32_dpp v22, v22, v22 row_half_mirror row_mask:0xf bank_mask:0xf bound_ctrl:1
	v_add_f32_dpp v23, v23, v23 row_half_mirror row_mask:0xf bank_mask:0xf bound_ctrl:1
	v_add_f32_dpp v24, v24, v24 row_half_mirror row_mask:0xf bank_mask:0xf bound_ctrl:1
	v_add_f32_dpp v25, v25, v25 row_half_mirror row_mask:0xf bank_mask:0xf bound_ctrl:1
	v_add_f32_dpp v26, v26, v26 row_half_mirror row_mask:0xf bank_mask:0xf bound_ctrl:1
	v_add_f32_dpp v6, v6, v6 row_half_mirror row_mask:0xf bank_mask:0xf bound_ctrl:1
	v_add_f32_dpp v7, v7, v7 row_half_mirror row_mask:0xf bank_mask:0xf bound_ctrl:1
	s_nop 1
	v_add_f32_dpp v10, v10, v10 row_mirror row_mask:0xf bank_mask:0xf bound_ctrl:1
	v_add_f32_dpp v11, v11, v11 row_mirror row_mask:0xf bank_mask:0xf bound_ctrl:1
	v_add_f32_dpp v12, v12, v12 row_mirror row_mask:0xf bank_mask:0xf bound_ctrl:1
	v_add_f32_dpp v13, v13, v13 row_mirror row_mask:0xf bank_mask:0xf bound_ctrl:1
	v_add_f32_dpp v14, v14, v14 row_mirror row_mask:0xf bank_mask:0xf bound_ctrl:1
	v_add_f32_dpp v15, v15, v15 row_mirror row_mask:0xf bank_mask:0xf bound_ctrl:1
	v_add_f32_dpp v16, v16, v16 row_mirror row_mask:0xf bank_mask:0xf bound_ctrl:1
	v_add_f32_dpp v17, v17, v17 row_mirror row_mask:0xf bank_mask:0xf bound_ctrl:1
	v_add_f32_dpp v18, v18, v18 row_mirror row_mask:0xf bank_mask:0xf bound_ctrl:1
	v_add_f32_dpp v19, v19, v19 row_mirror row_mask:0xf bank_mask:0xf bound_ctrl:1
	v_add_f32_dpp v20, v20, v20 row_mirror row_mask:0xf bank_mask:0xf bound_ctrl:1
	v_add_f32_dpp v21, v21, v21 row_mirror row_mask:0xf bank_mask:0xf bound_ctrl:1
	v_add_f32_dpp v22, v22, v22 row_mirror row_mask:0xf bank_mask:0xf bound_ctrl:1
	v_add_f32_dpp v23, v23, v23 row_mirror row_mask:0xf bank_mask:0xf bound_ctrl:1
	v_add_f32_dpp v24, v24, v24 row_mirror row_mask:0xf bank_mask:0xf bound_ctrl:1
	v_add_f32_dpp v25, v25, v25 row_mirror row_mask:0xf bank_mask:0xf bound_ctrl:1
	v_add_f32_dpp v26, v26, v26 row_mirror row_mask:0xf bank_mask:0xf bound_ctrl:1
	v_add_f32_dpp v6, v6, v6 row_mirror row_mask:0xf bank_mask:0xf bound_ctrl:1
	v_add_f32_dpp v7, v7, v7 row_mirror row_mask:0xf bank_mask:0xf bound_ctrl:1
	s_and_saveexec_b64 s[2:3], s[40:41]
	s_cbranch_execz .LBB0_1320
	v_add_u32_e32 v8, s1, v139
	v_mov_b32_e32 v27, v0
	v_mov_b32_e32 v28, v0
	v_mov_b32_e32 v29, v0
	ds_write_b128 v8, v[10:13] offset:36864
	ds_write_b128 v8, v[14:17] offset:36880
	ds_write_b128 v8, v[18:21] offset:36896
	ds_write_b128 v8, v[22:25] offset:36912
	ds_write_b128 v8, v[26:29] offset:36928
	s_branch .LBB0_1320
.Lhb_1320:
	s_or_b64 exec, exec, s[2:3]
	v_add3_u32 v8, s1, v143, v144
	ds_write_b32 v8, v6 offset:46336
	v_add3_u32 v6, s1, v140, v144
	ds_write_b32 v6, v7 offset:46336

.Lhb_1322:
	s_mov_b32 s100, 0
	s_mov_b32 s101, 0
	s_add_i32 s20, s0, 2
	s_cmpk_gt_u32 s20, 0x7e
	s_cbranch_scc1 .Lhb_1324
	v_lshl_add_u64 v[18:19], v[44:45], 0, v[42:43]
	v_add_co_u32_e32 v20, vcc, 0x1a430000, v18
	v_lshl_add_u64 v[8:9], v[46:47], 0, v[42:43]
	s_nop 0
	v_addc_co_u32_e32 v21, vcc, 0, v19, vcc
	v_add_co_u32_e32 v6, vcc, 0x1a431000, v18
	s_nop 1
	v_addc_co_u32_e32 v7, vcc, 0, v19, vcc
	v_add_co_u32_e32 v10, vcc, 0x38410000, v8
	global_load_dwordx2 v[82:83], v[20:21], off
	global_load_dwordx2 v[100:101], v[20:21], off offset:2048
	global_load_dwordx2 v[80:81], v[6:7], off
	global_load_dwordx2 v[88:89], v[6:7], off offset:2048
	v_addc_co_u32_e32 v11, vcc, 0, v9, vcc
	v_add_co_u32_e32 v12, vcc, 0x3c410000, v8
	s_nop 1
	v_addc_co_u32_e32 v13, vcc, 0, v9, vcc
	v_add_co_u32_e32 v20, vcc, 0x1a432000, v18
	global_load_dwordx2 v[78:79], v[10:11], off
	global_load_dwordx2 v[84:85], v[12:13], off
	global_load_dwordx2 v[90:91], v[12:13], off offset:2048
	global_load_dwordx2 v[86:87], v[10:11], off offset:2048
	v_addc_co_u32_e32 v21, vcc, 0, v19, vcc
	v_add_co_u32_e32 v6, vcc, 0x1a433000, v18
	s_nop 1
	v_addc_co_u32_e32 v7, vcc, 0, v19, vcc
	v_add_co_u32_e32 v10, vcc, 0x1a434000, v18
	s_nop 1
	v_addc_co_u32_e32 v11, vcc, 0, v19, vcc
	global_load_dwordx2 v[102:103], v[20:21], off
	global_load_dwordx2 v[92:93], v[20:21], off offset:2048
	global_load_dwordx2 v[104:105], v[6:7], off offset:2048
	global_load_dwordx2 v[98:99], v[10:11], off
	v_add_co_u32_e32 v20, vcc, 0x38411000, v8
	s_nop 1
	v_addc_co_u32_e32 v21, vcc, 0, v9, vcc
	v_add_co_u32_e32 v6, vcc, 0x3c411000, v8
	s_nop 1
	v_addc_co_u32_e32 v7, vcc, 0, v9, vcc
	v_add_co_u32_e32 v18, vcc, 0x1a435000, v18
	global_load_dwordx2 v[94:95], v[20:21], off
	global_load_dwordx2 v[96:97], v[6:7], off
	v_addc_co_u32_e32 v19, vcc, 0, v19, vcc
	global_load_dwordx2 v[106:107], v[18:19], off
	s_mov_b32 s100, 1

.Lhb_1328:
	v_mov_b64_e32 v[18:19], v[2:3]
	s_andn2_b64 vcc, exec, s[2:3]
	v_mov_b64_e32 v[20:21], v[4:5]
	s_cbranch_vccnz .Lhb_1331
	s_add_i32 s30, s0, 1
	s_lshl_b64 s[2:3], s[30:31], 16
	v_lshl_add_u64 v[18:19], v[30:31], 0, s[2:3]
	global_load_dwordx4 v[18:21], v[18:19], off
	s_mov_b32 s101, 1
	s_cmp_lt_u32 s20, 2
	s_cbranch_scc0 .Lhb_1332

; __device__ __forceinline__ void unpk8(const u32x4 w, f32x4& a, f32x4& b) { a = (f32x4){bflo(w.x), bfhi(w.x), bflo(w.y), bfhi(w.y)}; b = (f32x4){bflo(w.z), bfhi(w.z), bflo(w.w), bfhi(w.w)}; }
; __device__ __forceinline__ u32x4 pk8(const f32x4 a, const f32x4 b) { u32x4 w; w.x = cvt_pk_bf16(a[0], a[1]); w.y = cvt_pk_bf16(a[2], a[3]); w.z = cvt_pk_bf16(b[0], b[1]); w.w = cvt_pk_bf16(b[2], b[3]); return w; }
; #define LAS __attribute__((address_space(3)))
; __device__ __forceinline__ void scan_unit(Frame& F, const Args& a, int layer, int unit) {
;     ...
;             if (it >= 2) {
;                 const LAS float* buf = bufs + (it & 1) * SC_BUF; const LAS float* yb = sY + (it & 1) * SC_VEC;
;                 const size_t row = (size_t)b * SEQ + (size_t)(it - 2) * SC + tl; const int o = tl * 64 + c8 * 8;
;                 f32x4 y_[2], v_[2], g_[2];
; #pragma unroll
;                 for (int i = 0; i < 2; ++i) { y_[i] = *(const LAS f32x4*)(yb + o + 4 * i); v_[i] = *(const LAS f32x4*)(buf + SC_VP + o + 4 * i); }
;                 const float bon = buf[SC_BON + tl * 8 + c8];
;                 unpk8(cur.gt, g_[0], g_[1]);
;                 const float s1 = ((y_[0].x + y_[0].y) + (y_[0].z + y_[0].w)) + ((y_[1].x + y_[1].y) + (y_[1].z + y_[1].w));
;                 const float mu = sum8(s1) * (1.f / 64.f);
;                 float s2 = 0.f;
; #pragma unroll
;                 for (int i = 0; i < 2; ++i) { y_[i] = y_[i] - mu; const f32x4 q = y_[i] * y_[i]; s2 += (q.x + q.y) + (q.z + q.w); }
;                 const float rstd = __builtin_amdgcn_rsqf(sum8(s2) * (1.f / 64.f) + 64e-5f);
;                 f32x4 o_[2];
; #pragma unroll
;                 for (int i = 0; i < 2; ++i) o_[i] = (y_[i] * rstd * *(const f32x4*)(a.in[14] + po + 4 * i) + *(const f32x4*)(a.in[15] + po + 4 * i) + bon * v_[i]) * g_[i];
;                 *(v4u*)(YA + row * 1024 + ch) = pk8(o_[0], o_[1]);
.Lhpb_g1:
	s_and_b32 s1, s20, 1
	s_mul_i32 s2, s1, 0xb900
	s_add_i32 s2, s2, 0
	v_lshl_add_u32 v10, s1, 13, v129
	v_lshl_add_u32 v6, v128, 2, s2
	ds_read_b128 v[14:17], v6 offset:38144
	ds_read_b128 v[6:9], v6 offset:38160
	ds_read_b128 v[22:25], v10
	ds_read_b128 v[10:13], v10 offset:16
	v_lshlrev_b32_e32 v26, 2, v126
	v_add3_u32 v26, s2, v141, v26
	v_lshlrev_b32_e32 v114, 16, v2
	v_and_b32_e32 v115, 0xffff0000, v2
	v_lshlrev_b32_e32 v116, 16, v3
	v_and_b32_e32 v117, 0xffff0000, v3
	v_lshlrev_b32_e32 v110, 16, v4
	v_and_b32_e32 v111, 0xffff0000, v4
	v_lshlrev_b32_e32 v112, 16, v5
	v_and_b32_e32 v113, 0xffff0000, v5
	s_waitcnt lgkmcnt(0)
	v_mov_b32_e32 v2, v22
	v_mov_b32_e32 v3, v10
	v_mov_b32_e32 v4, v23
	v_mov_b32_e32 v5, v11
	ds_read_b32 v108, v26 offset:46336
	v_pk_add_f32 v[2:3], v[2:3], v[4:5]
	v_mov_b32_e32 v4, v24
	v_mov_b32_e32 v5, v12
	v_mov_b32_e32 v26, v25
	v_mov_b32_e32 v27, v13
	v_pk_add_f32 v[4:5], v[4:5], v[26:27]
	s_mov_b32 s1, s31
	v_pk_add_f32 v[2:3], v[2:3], v[4:5]
	s_lshl_b64 s[2:3], s[0:1], 16
	v_add_f32_e32 v2, v2, v3
	s_nop 1
	v_add_f32_dpp v2, v2, v2 quad_perm:[1,0,3,2] row_mask:0xf bank_mask:0xf bound_ctrl:1
	s_nop 1
	v_add_f32_dpp v2, v2, v2 quad_perm:[2,3,0,1] row_mask:0xf bank_mask:0xf bound_ctrl:1
	s_nop 1
	v_add_f32_dpp v26, v2, v2 row_half_mirror row_mask:0xf bank_mask:0xf bound_ctrl:1
	v_fmamk_f32 v3, v26, 0xbc800000, v23
	v_fmamk_f32 v2, v26, 0xbc800000, v22
	v_fmamk_f32 v119, v26, 0xbc800000, v11
	v_fmamk_f32 v118, v26, 0xbc800000, v10
	v_fmamk_f32 v25, v26, 0xbc800000, v25
	v_fmac_f32_e32 v24, 0xbc800000, v26
	v_pk_mul_f32 v[22:23], v[2:3], v[2:3]
	v_fmamk_f32 v13, v26, 0xbc800000, v13
	v_fmac_f32_e32 v12, 0xbc800000, v26
	v_pk_mul_f32 v[26:27], v[118:119], v[118:119]
	v_pk_mul_f32 v[4:5], v[24:25], v[24:25]
	v_pk_mul_f32 v[10:11], v[12:13], v[12:13]
	v_mov_b32_e32 v28, v22
	v_mov_b32_e32 v29, v26
	v_mov_b32_e32 v26, v23
	v_pk_add_f32 v[22:23], v[28:29], v[26:27]
	v_mov_b32_e32 v26, v4
	v_mov_b32_e32 v27, v10
	v_mov_b32_e32 v10, v5
	v_pk_add_f32 v[10:11], v[26:27], v[10:11]
	s_nop 0
	v_pk_add_f32 v[10:11], v[22:23], v[10:11]
	s_nop 0
	v_add_f32_e32 v10, v10, v11
	s_nop 1
	v_add_f32_dpp v10, v10, v10 quad_perm:[1,0,3,2] row_mask:0xf bank_mask:0xf bound_ctrl:1
	s_nop 1
	v_add_f32_dpp v10, v10, v10 quad_perm:[2,3,0,1] row_mask:0xf bank_mask:0xf bound_ctrl:1
	s_nop 1
	v_add_f32_dpp v10, v10, v10 row_half_mirror row_mask:0xf bank_mask:0xf bound_ctrl:1
	v_fmamk_f32 v10, v10, 0x3c800000, v243
	v_rsq_f32_e32 v120, v10
	s_nop 0
	v_pk_mul_f32 v[10:11], v[2:3], v[120:121] op_sel_hi:[1,0]
	v_pk_mul_f32 v[122:123], v[24:25], v[120:121] op_sel_hi:[1,0]
	v_pk_mul_f32 v[12:13], v[12:13], v[120:121] op_sel_hi:[1,0]
	v_pk_fma_f32 v[28:29], v[178:179], v[122:123], v[186:187]
	v_pk_fma_f32 v[10:11], v[176:177], v[10:11], v[184:185]
	v_pk_fma_f32 v[12:13], v[182:183], v[12:13], v[190:191]
	s_waitcnt lgkmcnt(0)
	v_pk_fma_f32 v[14:15], v[14:15], v[108:109], v[10:11] op_sel_hi:[1,0,1]
	v_pk_fma_f32 v[10:11], v[16:17], v[108:109], v[28:29] op_sel_hi:[1,0,1]
	v_pk_mul_f32 v[16:17], v[118:119], v[120:121] op_sel_hi:[1,0]
	v_pk_mul_f32 v[14:15], v[14:15], v[114:115]
	v_pk_fma_f32 v[16:17], v[180:181], v[16:17], v[188:189]
	v_pk_mul_f32 v[10:11], v[10:11], v[116:117]
	v_pk_fma_f32 v[16:17], v[6:7], v[108:109], v[16:17] op_sel_hi:[1,0,1]
	v_pk_fma_f32 v[6:7], v[8:9], v[108:109], v[12:13] op_sel_hi:[1,0,1]
	v_pk_mul_f32 v[8:9], v[16:17], v[110:111]
	v_pk_mul_f32 v[6:7], v[6:7], v[112:113]
	v_cvt_pk_bf16_f32 v12, v14, v15
	v_cvt_pk_bf16_f32 v13, v10, v11
	v_cvt_pk_bf16_f32 v14, v8, v9
	s_nop 0
	v_cvt_pk_bf16_f32 v15, v6, v7
	v_lshl_add_u64 v[6:7], v[30:31], 0, s[2:3]
	global_store_dwordx4 v[6:7], v[12:15], off
	s_cmpk_gt_u32 s20, 0x7f
	s_cbranch_scc1 .Lhb_1321

; #define LAS __attribute__((address_space(3)))
; #define UNP4(W) ((f32x4){bflo((W).x), bfhi((W).x), bflo((W).y), bfhi((W).y)})
; #define EXP4(E) ((f32x4){__builtin_amdgcn_exp2f(-1.44269504f * (E).x), __builtin_amdgcn_exp2f(-1.44269504f * (E).y), __builtin_amdgcn_exp2f(-1.44269504f * (E).z), __builtin_amdgcn_exp2f(-1.44269504f * (E).w)})
; #define SUM16(X) sum16_ns(X)
; __device__ __forceinline__ void scan_unit(Frame& F, const Args& a, int layer, int unit) {
;     ...
;                 const f32x4 pkk_ = *(const f32x4*)(a.in[11] + pop), pka_ = *(const f32x4*)(a.in[12] + pop), prk_ = *(const f32x4*)(a.in[13] + pop);
;                 const f32x4 zk0 = UNP4(cur.k0), zk1 = UNP4(cur.k1), zk2 = UNP4(cur.k2), zk3 = UNP4(cur.k3);
;                 f32x4 kn0 = zk0 * pkk_, kn1 = zk1 * pkk_, kn2 = zk2 * pkk_, kn3 = zk3 * pkk_;
;                 kn0 = kn0 * __builtin_amdgcn_rsqf(fmaxf(SUM16(DOT4(kn0, kn0)), 1e-24f)); kn1 = kn1 * __builtin_amdgcn_rsqf(fmaxf(SUM16(DOT4(kn1, kn1)), 1e-24f));
;                 kn2 = kn2 * __builtin_amdgcn_rsqf(fmaxf(SUM16(DOT4(kn2, kn2)), 1e-24f)); kn3 = kn3 * __builtin_amdgcn_rsqf(fmaxf(SUM16(DOT4(kn3, kn3)), 1e-24f));
;                 const f32x4 r0 = UNP4(cur.r0), r1 = UNP4(cur.r1), v0 = UNP4(cur.v0), v1 = UNP4(cur.v1), v2 = UNP4(cur.v2);
;                 const f32x4 ar0 = UNP4(cur.a0), ar1 = UNP4(cur.a1), ar2 = UNP4(cur.a2);
;                 const f32x4 e0 = UNP4(cur.e0), e1 = UNP4(cur.e1), e2 = UNP4(cur.e2);
;                 const f32x4 w0 = EXP4(e0), w1 = EXP4(e1), w2 = EXP4(e2);
;                 const f32x4 a1v = -kn1, a2v = -kn2, a3v = -kn3;
;                 const f32x4 b0 = kn0 * ar0, b1 = kn1 * ar1, b2 = kn2 * ar2;
;                 const f32x4 kp0 = zk0 * (1.f + (ar0 - 1.f) * pka_), kp1 = zk1 * (1.f + (ar1 - 1.f) * pka_), kp2 = zk2 * (1.f + (ar2 - 1.f) * pka_);
;                 const f32x4 W2 = w0 * w1, Bt = b0 * w1, Kt = kp0 * w1, x0v = a2v, x1v = w2 * a3v;
;                 const f32x4 X0 = W2 * x0v, X1 = W2 * x1v, X2 = w0 * r0, X3 = W2 * r1;
;                 *(LAS f32x4*)(buf + SC_WW + pr * 64 + c4 * 4) = W2;
.Lhpb_g2:
	s_nop 1
	v_mov_b64_e32 v[14:15], v[192:193]
	v_mov_b64_e32 v[16:17], v[194:195]
	v_mov_b64_e32 v[10:11], v[196:197]
	v_mov_b64_e32 v[12:13], v[198:199]
	v_mov_b64_e32 v[6:7], v[200:201]
	v_mov_b64_e32 v[8:9], v[202:203]
	v_lshlrev_b32_e32 v118, 16, v50
	v_and_b32_e32 v119, 0xffff0000, v50
	v_lshlrev_b32_e32 v120, 16, v51
	v_and_b32_e32 v121, 0xffff0000, v51
	v_lshlrev_b32_e32 v108, 16, v70
	v_and_b32_e32 v109, 0xffff0000, v70
	v_lshlrev_b32_e32 v116, 16, v71
	v_and_b32_e32 v117, 0xffff0000, v71
	v_lshlrev_b32_e32 v112, 16, v64
	v_and_b32_e32 v113, 0xffff0000, v64
	v_lshlrev_b32_e32 v114, 16, v65
	v_and_b32_e32 v115, 0xffff0000, v65
	v_lshlrev_b32_e32 v2, 16, v76
	v_and_b32_e32 v3, 0xffff0000, v76
	v_lshlrev_b32_e32 v4, 16, v77
	v_and_b32_e32 v5, 0xffff0000, v77
	v_and_b32_e32 v156, 0xffff0000, v66
	v_lshlrev_b32_e32 v158, 16, v67
	v_and_b32_e32 v160, 0xffff0000, v67
	v_lshlrev_b32_e32 v67, 16, v63
	v_and_b32_e32 v63, 0xffff0000, v63
	v_and_b32_e32 v149, 0xffff0000, v49
	s_bitcmp1_b32 s20, 0
	v_and_b32_e32 v151, 0xffff0000, v68
	v_lshlrev_b32_e32 v152, 16, v69
	v_and_b32_e32 v153, 0xffff0000, v69
	v_lshlrev_b32_e32 v150, 16, v68
	v_lshlrev_b32_e32 v68, 16, v60
	v_and_b32_e32 v69, 0xffff0000, v60
	v_lshlrev_b32_e32 v60, 16, v61
	v_and_b32_e32 v61, 0xffff0000, v61
	v_lshlrev_b32_e32 v154, 16, v74
	v_and_b32_e32 v155, 0xffff0000, v74
	v_lshlrev_b32_e32 v74, 16, v75
	v_and_b32_e32 v75, 0xffff0000, v75
	s_cselect_b32 s1, 0xb900, 0
	s_add_i32 s1, s1, 0
	v_mov_b32_e32 v157, v0
	v_mov_b32_e32 v159, v0
	v_mov_b32_e32 v161, v0
	v_pk_mul_f32 v[22:23], v[14:15], v[118:119]
	v_pk_mul_f32 v[24:25], v[16:17], v[120:121]
	v_pk_mul_f32 v[26:27], v[14:15], v[108:109]
	v_pk_mul_f32 v[28:29], v[16:17], v[116:117]
	v_pk_mul_f32 v[50:51], v[14:15], v[112:113]
	v_pk_mul_f32 v[70:71], v[16:17], v[114:115]
	v_pk_mul_f32 v[4:5], v[16:17], v[4:5]
	v_pk_mul_f32 v[2:3], v[14:15], v[2:3]
	v_pk_mul_f32 v[14:15], v[24:25], v[24:25]
	v_pk_mul_f32 v[16:17], v[22:23], v[22:23]
	v_pk_mul_f32 v[64:65], v[28:29], v[28:29]
	v_pk_mul_f32 v[76:77], v[26:27], v[26:27]
	v_pk_mov_b32 v[146:147], v[16:17], v[14:15] op_sel:[1,0]
	v_mov_b32_e32 v17, v15
	v_pk_mov_b32 v[14:15], v[76:77], v[64:65] op_sel:[1,0]
	v_mov_b32_e32 v77, v65
	v_pk_mul_f32 v[110:111], v[70:71], v[70:71]
	v_pk_mul_f32 v[122:123], v[50:51], v[50:51]
	v_pk_add_f32 v[16:17], v[146:147], v[16:17]
	v_pk_add_f32 v[14:15], v[14:15], v[76:77]
	v_pk_mov_b32 v[64:65], v[122:123], v[110:111] op_sel:[1,0]
	v_mov_b32_e32 v123, v111
	v_add_f32_e32 v16, v16, v17
	v_add_f32_e32 v14, v14, v15
	v_mul_f32_e32 v145, v3, v3
	v_mul_f32_e32 v148, v5, v5
	v_pk_add_f32 v[64:65], v[64:65], v[122:123]
	v_add_f32_dpp v16, v16, v16 quad_perm:[1,0,3,2] row_mask:0xf bank_mask:0xf bound_ctrl:1
	v_add_f32_dpp v14, v14, v14 quad_perm:[1,0,3,2] row_mask:0xf bank_mask:0xf bound_ctrl:1
	v_fmac_f32_e32 v145, v2, v2
	v_fmac_f32_e32 v148, v4, v4
	v_add_f32_e32 v15, v64, v65
	v_add_f32_e32 v76, v145, v148
	v_lshlrev_b32_e32 v122, 16, v66
	v_add_f32_dpp v15, v15, v15 quad_perm:[1,0,3,2] row_mask:0xf bank_mask:0xf bound_ctrl:1
	v_add_f32_dpp v16, v16, v16 quad_perm:[2,3,0,1] row_mask:0xf bank_mask:0xf bound_ctrl:1
	v_add_f32_dpp v14, v14, v14 quad_perm:[2,3,0,1] row_mask:0xf bank_mask:0xf bound_ctrl:1
	v_add_f32_dpp v17, v76, v76 quad_perm:[1,0,3,2] row_mask:0xf bank_mask:0xf bound_ctrl:1
	v_lshlrev_b32_e32 v66, 16, v62
	v_and_b32_e32 v62, 0xffff0000, v62
	v_add_f32_dpp v15, v15, v15 quad_perm:[2,3,0,1] row_mask:0xf bank_mask:0xf bound_ctrl:1
	v_add_f32_dpp v16, v16, v16 row_half_mirror row_mask:0xf bank_mask:0xf bound_ctrl:1
	v_add_f32_dpp v14, v14, v14 row_half_mirror row_mask:0xf bank_mask:0xf bound_ctrl:1
	v_add_f32_dpp v17, v17, v17 quad_perm:[2,3,0,1] row_mask:0xf bank_mask:0xf bound_ctrl:1
	v_lshlrev_b32_e32 v110, 16, v73
	v_and_b32_e32 v73, 0xffff0000, v73
	v_add_f32_dpp v15, v15, v15 row_half_mirror row_mask:0xf bank_mask:0xf bound_ctrl:1
	v_add_f32_dpp v16, v16, v16 row_mirror row_mask:0xf bank_mask:0xf bound_ctrl:1
	v_add_f32_dpp v14, v14, v14 row_mirror row_mask:0xf bank_mask:0xf bound_ctrl:1
	v_add_f32_dpp v17, v17, v17 row_half_mirror row_mask:0xf bank_mask:0xf bound_ctrl:1
	v_lshlrev_b32_e32 v146, 16, v48
	v_max_f32_e32 v16, v16, v16
	v_add_f32_dpp v15, v15, v15 row_mirror row_mask:0xf bank_mask:0xf bound_ctrl:1
	v_max_f32_e32 v14, v14, v14
	v_add_f32_dpp v77, v17, v17 row_mirror row_mask:0xf bank_mask:0xf bound_ctrl:1
	v_max_f32_e32 v16, 0x179abe15, v16
	v_max_f32_e32 v17, 0x179abe15, v14
	v_max_f32_e32 v15, v15, v15
	v_rsq_f32_e32 v14, v16
	v_rsq_f32_e32 v16, v17
	v_max_f32_e32 v15, 0x179abe15, v15
	v_rsq_f32_e32 v76, v15
	v_pk_mul_f32 v[64:65], v[26:27], v[16:17] op_sel_hi:[1,0]
	v_pk_mul_f32 v[26:27], v[28:29], v[16:17] op_sel_hi:[1,0]
	v_max_f32_e32 v28, v77, v77
	v_max_f32_e32 v28, 0x179abe15, v28
	v_pk_mul_f32 v[24:25], v[24:25], v[14:15] op_sel_hi:[1,0]
	v_pk_mul_f32 v[22:23], v[22:23], v[14:15] op_sel_hi:[1,0]
	v_pk_mul_f32 v[16:17], v[50:51], v[76:77] op_sel_hi:[1,0]
	v_pk_mul_f32 v[14:15], v[70:71], v[76:77] op_sel_hi:[1,0]
	v_rsq_f32_e32 v76, v28
	v_lshlrev_b32_e32 v28, 16, v54
	v_and_b32_e32 v29, 0xffff0000, v54
	v_lshlrev_b32_e32 v54, 16, v58
	v_and_b32_e32 v58, 0xffff0000, v58
	v_lshlrev_b32_e32 v50, 16, v52
	v_and_b32_e32 v51, 0xffff0000, v52
	v_lshlrev_b32_e32 v70, 16, v53
	v_and_b32_e32 v71, 0xffff0000, v53
	v_lshlrev_b32_e32 v52, 16, v55
	v_and_b32_e32 v53, 0xffff0000, v55
	v_lshlrev_b32_e32 v55, 16, v59
	v_mul_f32_e32 v58, 0xbfb8aa3b, v58
	v_and_b32_e32 v59, 0xffff0000, v59
	v_exp_f32_e32 v163, v58
	v_mul_f32_e32 v58, 0xbfb8aa3b, v55
	v_exp_f32_e32 v164, v58
	v_mul_f32_e32 v58, 0xbfb8aa3b, v59
	v_exp_f32_e32 v165, v58
; #define LAS __attribute__((address_space(3)))
; #define SUM16(X) sum16_ns(X)
; __device__ __forceinline__ void scan_unit(Frame& F, const Args& a, int layer, int unit) {
;     ...
;                 const f32x4 w0 = EXP4(e0), w1 = EXP4(e1), w2 = EXP4(e2);
;                 const f32x4 a1v = -kn1, a2v = -kn2, a3v = -kn3;
;                 const f32x4 b0 = kn0 * ar0, b1 = kn1 * ar1, b2 = kn2 * ar2;
;                 const f32x4 kp0 = zk0 * (1.f + (ar0 - 1.f) * pka_), kp1 = zk1 * (1.f + (ar1 - 1.f) * pka_), kp2 = zk2 * (1.f + (ar2 - 1.f) * pka_);
;                 const f32x4 W2 = w0 * w1, Bt = b0 * w1, Kt = kp0 * w1, x0v = a2v, x1v = w2 * a3v;
;                 const f32x4 X0 = W2 * x0v, X1 = W2 * x1v, X2 = w0 * r0, X3 = W2 * r1;
;                 *(LAS f32x4*)(buf + SC_WW + pr * 64 + c4 * 4) = W2;
;                 *(LAS f32x4*)(buf + SC_VP + (2 * pr) * 64 + c4 * 4) = v0; *(LAS f32x4*)(buf + SC_VP + (2 * pr + 1) * 64 + c4 * 4) = v1;
;                 { LAS f32x4* vq = (LAS f32x4*)(buf + SC_VQ + pr * 256 + c4 * 16);
;                   vq[0] = (f32x4){v0.x, v1.x, v2.x, 0.f}; vq[1] = (f32x4){v0.y, v1.y, v2.y, 0.f}; vq[2] = (f32x4){v0.z, v1.z, v2.z, 0.f}; vq[3] = (f32x4){v0.w, v1.w, v2.w, 0.f}; }
;                 { LAS v2u* bkp = (LAS v2u*)(buf + SC_BK + pr * 128) + (((c4 & 3) * 4) * 4 + (c4 >> 2));
;                   bkp[0] = (v2u){cvt_pk_bf16(Bt.x, Kt.x), cvt_pk_bf16(b1.x, kp1.x)}; bkp[4] = (v2u){cvt_pk_bf16(Bt.y, Kt.y), cvt_pk_bf16(b1.y, kp1.y)};
;                   bkp[8] = (v2u){cvt_pk_bf16(Bt.z, Kt.z), cvt_pk_bf16(b1.z, kp1.z)}; bkp[12] = (v2u){cvt_pk_bf16(Bt.w, Kt.w), cvt_pk_bf16(b1.w, kp1.w)}; }
;                 { LAS unsigned char* xp = (LAS unsigned char*)(buf + SC_XA) + pr * 512 + (c4 >> 3) * 64 + (c4 & 3) * 16 + ((c4 >> 2) & 1) * 8;
;                   *(LAS v2u*)xp = (v2u){cvt_pk_bf16(X0.x, X0.y), cvt_pk_bf16(X0.z, X0.w)}; *(LAS v2u*)(xp + 128) = (v2u){cvt_pk_bf16(X1.x, X1.y), cvt_pk_bf16(X1.z, X1.w)};
;                   *(LAS v2u*)(xp + 256) = (v2u){cvt_pk_bf16(X2.x, X2.y), cvt_pk_bf16(X2.z, X2.w)}; *(LAS v2u*)(xp + 384) = (v2u){cvt_pk_bf16(X3.x, X3.y), cvt_pk_bf16(X3.z, X3.w)}; }
;                 const f32x4 ca = (f32x4){SUM16(DOT4(Bt, x0v)), SUM16(DOT4(Kt, x0v)), SUM16(DOT4(b1, x0v)), SUM16(DOT4(kp1, x0v))};
;                 const f32x4 cb = (f32x4){SUM16(DOT4(Bt, x1v)), SUM16(DOT4(Kt, x1v)), SUM16(DOT4(b1, x1v)), SUM16(DOT4(kp1, x1v))};
	v_mul_f32_e32 v58, 0xbfb8aa3b, v66
	v_exp_f32_e32 v166, v58
	v_mul_f32_e32 v58, 0xbfb8aa3b, v62
	v_exp_f32_e32 v167, v58
	v_mul_f32_e32 v58, 0xbfb8aa3b, v67
	v_lshlrev_b32_e32 v77, 16, v72
	v_exp_f32_e32 v168, v58
	v_mul_f32_e32 v58, 0xbfb8aa3b, v63
	v_and_b32_e32 v72, 0xffff0000, v72
	v_exp_f32_e32 v169, v58
	v_mul_f32_e32 v58, 0xbfb8aa3b, v77
	v_exp_f32_e32 v170, v58
	v_mul_f32_e32 v58, 0xbfb8aa3b, v72
	v_exp_f32_e32 v171, v58
	v_mul_f32_e32 v58, 0xbfb8aa3b, v110
	v_and_b32_e32 v147, 0xffff0000, v48
	v_lshlrev_b32_e32 v148, 16, v49
	v_lshlrev_b32_e32 v48, 16, v56
	v_and_b32_e32 v49, 0xffff0000, v56
	v_mul_f32_e32 v54, 0xbfb8aa3b, v54
	v_exp_f32_e32 v172, v58
	v_mul_f32_e32 v58, 0xbfb8aa3b, v73
	v_lshlrev_b32_e32 v56, 16, v57
	v_and_b32_e32 v57, 0xffff0000, v57
	v_exp_f32_e32 v162, v54
	v_exp_f32_e32 v173, v58
	v_pk_add_f32 v[58:59], v[48:49], -1.0 op_sel_hi:[1,0]
	v_pk_mul_f32 v[66:67], v[4:5], v[76:77] op_sel_hi:[1,0] neg_lo:[0,1] neg_hi:[0,1]
	v_pk_mul_f32 v[4:5], v[22:23], v[48:49]
	v_pk_add_f32 v[48:49], v[56:57], -1.0 op_sel_hi:[1,0]
	v_pk_fma_f32 v[58:59], v[58:59], v[10:11], 1.0 op_sel_hi:[1,1,0]
	v_pk_mul_f32 v[22:23], v[24:25], v[56:57]
	v_pk_mul_f32 v[24:25], v[26:27], v[60:61]
	v_pk_mul_f32 v[54:55], v[64:65], v[68:69]
	v_pk_fma_f32 v[56:57], v[48:49], v[12:13], 1.0 op_sel_hi:[1,1,0]
	v_pk_mul_f32 v[48:49], v[58:59], v[118:119]
	v_pk_add_f32 v[58:59], v[60:61], -1.0 op_sel_hi:[1,0]
	v_pk_add_f32 v[62:63], v[68:69], -1.0 op_sel_hi:[1,0]
	v_pk_add_f32 v[60:61], v[74:75], -1.0 op_sel_hi:[1,0]
	v_pk_add_f32 v[68:69], v[154:155], -1.0 op_sel_hi:[1,0]
	v_pk_mul_f32 v[56:57], v[56:57], v[120:121]
	v_pk_fma_f32 v[62:63], v[62:63], v[10:11], 1.0 op_sel_hi:[1,1,0]
	v_pk_fma_f32 v[58:59], v[58:59], v[12:13], 1.0 op_sel_hi:[1,1,0]
	v_pk_fma_f32 v[10:11], v[68:69], v[10:11], 1.0 op_sel_hi:[1,1,0]
	v_pk_fma_f32 v[12:13], v[60:61], v[12:13], 1.0 op_sel_hi:[1,1,0]
	v_lshlrev_b32_e32 v120, 2, v127
	v_pk_mul_f32 v[76:77], v[2:3], v[76:77] op_sel_hi:[1,0] neg_lo:[0,1] neg_hi:[0,1]
	v_pk_mul_f32 v[58:59], v[58:59], v[116:117]
	v_pk_mul_f32 v[62:63], v[62:63], v[108:109]
	v_pk_mul_f32 v[108:109], v[12:13], v[114:115]
	v_pk_mul_f32 v[112:113], v[10:11], v[112:113]
	v_pk_mul_f32 v[12:13], v[168:169], v[164:165]
	v_pk_mul_f32 v[10:11], v[166:167], v[162:163]
	v_pk_mul_f32 v[116:117], v[172:173], v[66:67]
	v_add3_u32 v121, s1, v130, v120
	v_pk_mul_f32 v[72:73], v[168:169], v[22:23]
	v_pk_mul_f32 v[60:61], v[168:169], v[56:57]
	v_pk_mul_f32 v[114:115], v[170:171], v[76:77]
	v_pk_mul_f32 v[118:119], v[12:13], v[14:15] neg_lo:[0,1] neg_hi:[0,1]
	v_pk_mul_f32 v[168:169], v[12:13], v[116:117]
	v_pk_mul_f32 v[172:173], v[52:53], v[12:13]
	ds_write_b128 v121, v[10:13]
	v_add_u32_e32 v12, s1, v131
	v_pk_mul_f32 v[2:3], v[14:15], v[74:75]
	v_pk_mul_f32 v[74:75], v[166:167], v[4:5]
	v_pk_mul_f32 v[68:69], v[166:167], v[48:49]
	v_pk_mul_f32 v[166:167], v[10:11], v[16:17] neg_lo:[0,1] neg_hi:[0,1]
	v_pk_mul_f32 v[170:171], v[10:11], v[114:115]
	v_pk_mul_f32 v[174:175], v[28:29], v[10:11]
	v_add_u32_e32 v10, v12, v120
	ds_write_b128 v10, v[146:149] offset:38144
	v_add3_u32 v10, s1, v132, v120
	v_pk_mul_f32 v[110:111], v[16:17], v[154:155]
	ds_write_b128 v10, v[150:153] offset:38144
	v_add3_u32 v10, s1, v133, v134
	v_mov_b32_e32 v154, v147
	v_mov_b32_e32 v155, v151
	ds_write_b128 v10, v[154:157] offset:4112
	v_mov_b32_e32 v156, v148
	v_mov_b32_e32 v157, v152
	v_mov_b32_e32 v120, v146
	v_mov_b32_e32 v121, v150
	v_mov_b32_e32 v123, v0
	ds_write_b128 v10, v[156:159] offset:4128
	v_mov_b32_e32 v158, v149
	v_mov_b32_e32 v159, v153
	ds_write_b128 v10, v[120:123] offset:4096
	ds_write_b128 v10, v[158:161] offset:4144
	v_add3_u32 v13, v12, v135, v142
	v_cvt_pk_bf16_f32 v10, v74, v68
	v_cvt_pk_bf16_f32 v11, v54, v62
	ds_write_b64 v13, v[10:11] offset:20480
	v_cvt_pk_bf16_f32 v10, v75, v69
	v_cvt_pk_bf16_f32 v11, v55, v63
	ds_write_b64 v13, v[10:11] offset:20512
	v_cvt_pk_bf16_f32 v10, v72, v60
	v_cvt_pk_bf16_f32 v11, v24, v58
	ds_write_b64 v13, v[10:11] offset:20544
	v_cvt_pk_bf16_f32 v10, v73, v61
	v_cvt_pk_bf16_f32 v11, v25, v59
	ds_write_b64 v13, v[10:11] offset:20576
	v_add_u32_e32 v10, v12, v136
	v_add3_u32 v12, v10, v137, v138
	v_cvt_pk_bf16_f32 v10, v166, v167
	v_cvt_pk_bf16_f32 v11, v118, v119
	ds_write_b64 v12, v[10:11] offset:28672
	v_cvt_pk_bf16_f32 v10, v170, v171
	v_cvt_pk_bf16_f32 v11, v168, v169
	v_pk_mul_f32 v[164:165], v[164:165], v[70:71]
	v_pk_mul_f32 v[162:163], v[162:163], v[50:51]
	ds_write_b64 v12, v[10:11] offset:28800
	v_cvt_pk_bf16_f32 v10, v162, v163
	v_cvt_pk_bf16_f32 v11, v164, v165
	ds_write_b64 v12, v[10:11] offset:28928
	v_cvt_pk_bf16_f32 v10, v174, v175
	v_cvt_pk_bf16_f32 v11, v172, v173
	ds_write_b64 v12, v[10:11] offset:29056
	v_mul_f32_e64 v10, v75, -v17
	v_mul_f32_e64 v11, v73, -v15
	v_fma_f32 v10, v74, -v16, v10
	v_fma_f32 v11, v72, -v14, v11
	v_add_f32_e32 v10, v10, v11
	v_mul_f32_e64 v11, v69, -v17
	v_mul_f32_e64 v12, v61, -v15
	v_fma_f32 v11, v68, -v16, v11
	v_fma_f32 v12, v60, -v14, v12
	v_add_f32_e32 v11, v11, v12
	v_mul_f32_e64 v12, v55, -v17
	v_mul_f32_e64 v13, v25, -v15
	v_fma_f32 v12, v54, -v16, v12
	v_fma_f32 v13, v24, -v14, v13
	v_add_f32_e32 v12, v12, v13
	v_mul_f32_e64 v13, v63, -v17
	v_mul_f32_e64 v15, v59, -v15
	v_fma_f32 v13, v62, -v16, v13
	v_fma_f32 v14, v58, -v14, v15
	v_add_f32_e32 v13, v13, v14
	v_mul_f32_e32 v14, v75, v115
	v_mul_f32_e32 v15, v73, v117
	v_fmac_f32_e32 v14, v74, v114
	v_fmac_f32_e32 v15, v72, v116
	v_add_f32_e32 v14, v14, v15
	v_mul_f32_e32 v15, v69, v115
	v_mul_f32_e32 v16, v61, v117
	v_mul_f32_e32 v5, v5, v51
	v_fmac_f32_e32 v15, v68, v114
	v_fmac_f32_e32 v16, v60, v116
	v_fmac_f32_e32 v5, v4, v50
; #define SUM16(X) sum16_ns(X)
; __device__ __forceinline__ void scan_unit(Frame& F, const Args& a, int layer, int unit) {
;     ...
;                 const f32x4 ca = (f32x4){SUM16(DOT4(Bt, x0v)), SUM16(DOT4(Kt, x0v)), SUM16(DOT4(b1, x0v)), SUM16(DOT4(kp1, x0v))};
;                 const f32x4 cb = (f32x4){SUM16(DOT4(Bt, x1v)), SUM16(DOT4(Kt, x1v)), SUM16(DOT4(b1, x1v)), SUM16(DOT4(kp1, x1v))};
;                 const f32x4 cc = (f32x4){SUM16(DOT4(b2, a3v)), SUM16(DOT4(kp2, a3v)), SUM16(DOT4(b0, r0)), SUM16(DOT4(kp0, r0))};
;                 const f32x4 cd = (f32x4){SUM16(DOT4(Bt, r1)), SUM16(DOT4(Kt, r1)), SUM16(DOT4(b1, r1)), SUM16(DOT4(kp1, r1))};
;                 const float ci = SUM16(DOT4(kp0, a1v));
;                 const f32x4 z0 = r0 * kp0 * prk_, z1 = r1 * kp1 * prk_;
;                 const float bon0 = SUM16((z0.x + z0.y) + (z0.z + z0.w)), bon1 = SUM16((z1.x + z1.y) + (z1.z + z1.w));
	v_mul_f32_e32 v4, v23, v71
	v_add_f32_e32 v15, v15, v16
	v_mul_f32_e32 v16, v55, v115
	v_mul_f32_e32 v17, v25, v117
	v_fmac_f32_e32 v4, v22, v70
	v_mul_f32_e32 v55, v55, v29
	v_mul_f32_e32 v25, v25, v53
	v_add_f32_e32 v4, v5, v4
	v_mul_f32_e32 v5, v49, v51
	v_mul_f32_e32 v22, v57, v71
	v_fmac_f32_e32 v55, v54, v28
	v_fmac_f32_e32 v25, v24, v52
	v_fmac_f32_e32 v16, v54, v114
	v_fmac_f32_e32 v17, v24, v116
	v_fmac_f32_e32 v5, v48, v50
	v_fmac_f32_e32 v22, v56, v70
	v_add_f32_e32 v24, v55, v25
	v_mul_f32_e32 v25, v63, v29
	v_mul_f32_e32 v54, v59, v53
	v_add_f32_e32 v5, v5, v22
	v_mul_f32_e32 v22, v75, v29
	v_mul_f32_e32 v23, v73, v53
	v_fmac_f32_e32 v25, v62, v28
	v_fmac_f32_e32 v54, v58, v52
	v_add_f32_e32 v16, v16, v17
	v_mul_f32_e32 v17, v63, v115
	v_fmac_f32_e32 v22, v74, v28
	v_fmac_f32_e32 v23, v72, v52
	v_add_f32_e32 v25, v25, v54
	v_mul_f32_e64 v54, v49, -v65
	v_mul_f32_e64 v27, v57, -v27
	v_fmac_f32_e32 v17, v62, v114
	v_mul_f32_e32 v114, v59, v117
	v_mul_f32_e32 v111, v111, v77
	v_mul_f32_e32 v3, v3, v67
	v_add_f32_e32 v22, v22, v23
	v_mul_f32_e32 v23, v69, v29
	v_fma_f32 v54, v48, -v64, v54
	v_fma_f32 v26, v56, -v26, v27
	v_pk_mul_f32 v[48:49], v[50:51], v[48:49]
	v_pk_mul_f32 v[56:57], v[70:71], v[56:57]
	v_fmac_f32_e32 v114, v58, v116
	v_fmac_f32_e32 v111, v110, v76
	v_fmac_f32_e32 v3, v2, v66
	v_fmac_f32_e32 v23, v68, v28
	v_pk_mul_f32 v[56:57], v[8:9], v[56:57]
	v_pk_mul_f32 v[48:49], v[6:7], v[48:49]
	v_pk_mul_f32 v[28:29], v[28:29], v[62:63]
	v_pk_mul_f32 v[58:59], v[52:53], v[58:59]
	v_add_f32_e32 v2, v111, v3
	v_mul_f32_e32 v3, v113, v77
	v_mul_f32_e32 v67, v109, v67
	v_mul_f32_e32 v61, v61, v53
	v_pk_mul_f32 v[8:9], v[8:9], v[58:59]
	v_pk_mul_f32 v[28:29], v[6:7], v[28:29]
	v_add_f32_e32 v6, v48, v49
	v_add_f32_e32 v7, v56, v57
	v_fmac_f32_e32 v3, v112, v76
	v_fmac_f32_e32 v67, v108, v66
	v_fmac_f32_e32 v61, v60, v52
	v_add_f32_e32 v6, v6, v7
	v_add_f32_e32 v7, v28, v29
	v_add_f32_e32 v8, v8, v9
	v_add_f32_e32 v17, v17, v114
	v_add_f32_e32 v3, v3, v67
	v_add_f32_e32 v23, v23, v61
	v_add_f32_e32 v26, v54, v26
	v_add_f32_e32 v7, v7, v8
	v_add_f32_dpp v10, v10, v10 quad_perm:[1,0,3,2] row_mask:0xf bank_mask:0xf bound_ctrl:1
	v_add_f32_dpp v11, v11, v11 quad_perm:[1,0,3,2] row_mask:0xf bank_mask:0xf bound_ctrl:1
	v_add_f32_dpp v12, v12, v12 quad_perm:[1,0,3,2] row_mask:0xf bank_mask:0xf bound_ctrl:1
	v_add_f32_dpp v13, v13, v13 quad_perm:[1,0,3,2] row_mask:0xf bank_mask:0xf bound_ctrl:1
	v_add_f32_dpp v14, v14, v14 quad_perm:[1,0,3,2] row_mask:0xf bank_mask:0xf bound_ctrl:1
	v_add_f32_dpp v15, v15, v15 quad_perm:[1,0,3,2] row_mask:0xf bank_mask:0xf bound_ctrl:1
	v_add_f32_dpp v16, v16, v16 quad_perm:[1,0,3,2] row_mask:0xf bank_mask:0xf bound_ctrl:1
	v_add_f32_dpp v17, v17, v17 quad_perm:[1,0,3,2] row_mask:0xf bank_mask:0xf bound_ctrl:1
	v_add_f32_dpp v2, v2, v2 quad_perm:[1,0,3,2] row_mask:0xf bank_mask:0xf bound_ctrl:1
	v_add_f32_dpp v3, v3, v3 quad_perm:[1,0,3,2] row_mask:0xf bank_mask:0xf bound_ctrl:1
	v_add_f32_dpp v4, v4, v4 quad_perm:[1,0,3,2] row_mask:0xf bank_mask:0xf bound_ctrl:1
	v_add_f32_dpp v5, v5, v5 quad_perm:[1,0,3,2] row_mask:0xf bank_mask:0xf bound_ctrl:1
	v_add_f32_dpp v22, v22, v22 quad_perm:[1,0,3,2] row_mask:0xf bank_mask:0xf bound_ctrl:1
	v_add_f32_dpp v23, v23, v23 quad_perm:[1,0,3,2] row_mask:0xf bank_mask:0xf bound_ctrl:1
	v_add_f32_dpp v24, v24, v24 quad_perm:[1,0,3,2] row_mask:0xf bank_mask:0xf bound_ctrl:1
	v_add_f32_dpp v25, v25, v25 quad_perm:[1,0,3,2] row_mask:0xf bank_mask:0xf bound_ctrl:1
	v_add_f32_dpp v26, v26, v26 quad_perm:[1,0,3,2] row_mask:0xf bank_mask:0xf bound_ctrl:1
	v_add_f32_dpp v6, v6, v6 quad_perm:[1,0,3,2] row_mask:0xf bank_mask:0xf bound_ctrl:1
	v_add_f32_dpp v7, v7, v7 quad_perm:[1,0,3,2] row_mask:0xf bank_mask:0xf bound_ctrl:1
	s_nop 1
	v_add_f32_dpp v10, v10, v10 quad_perm:[2,3,0,1] row_mask:0xf bank_mask:0xf bound_ctrl:1
	v_add_f32_dpp v11, v11, v11 quad_perm:[2,3,0,1] row_mask:0xf bank_mask:0xf bound_ctrl:1
	v_add_f32_dpp v12, v12, v12 quad_perm:[2,3,0,1] row_mask:0xf bank_mask:0xf bound_ctrl:1
	v_add_f32_dpp v13, v13, v13 quad_perm:[2,3,0,1] row_mask:0xf bank_mask:0xf bound_ctrl:1
	v_add_f32_dpp v14, v14, v14 quad_perm:[2,3,0,1] row_mask:0xf bank_mask:0xf bound_ctrl:1
	v_add_f32_dpp v15, v15, v15 quad_perm:[2,3,0,1] row_mask:0xf bank_mask:0xf bound_ctrl:1
	v_add_f32_dpp v16, v16, v16 quad_perm:[2,3,0,1] row_mask:0xf bank_mask:0xf bound_ctrl:1
	v_add_f32_dpp v17, v17, v17 quad_perm:[2,3,0,1] row_mask:0xf bank_mask:0xf bound_ctrl:1
; #define LAS __attribute__((address_space(3)))
; #define SUM16(X) sum16_ns(X)
; __device__ __forceinline__ void scan_unit(Frame& F, const Args& a, int layer, int unit) {
;     ...
;                 const f32x4 ca = (f32x4){SUM16(DOT4(Bt, x0v)), SUM16(DOT4(Kt, x0v)), SUM16(DOT4(b1, x0v)), SUM16(DOT4(kp1, x0v))};
;                 const f32x4 cb = (f32x4){SUM16(DOT4(Bt, x1v)), SUM16(DOT4(Kt, x1v)), SUM16(DOT4(b1, x1v)), SUM16(DOT4(kp1, x1v))};
;                 const f32x4 cc = (f32x4){SUM16(DOT4(b2, a3v)), SUM16(DOT4(kp2, a3v)), SUM16(DOT4(b0, r0)), SUM16(DOT4(kp0, r0))};
;                 const f32x4 cd = (f32x4){SUM16(DOT4(Bt, r1)), SUM16(DOT4(Kt, r1)), SUM16(DOT4(b1, r1)), SUM16(DOT4(kp1, r1))};
;                 const float ci = SUM16(DOT4(kp0, a1v));
;                 const f32x4 z0 = r0 * kp0 * prk_, z1 = r1 * kp1 * prk_;
;                 const float bon0 = SUM16((z0.x + z0.y) + (z0.z + z0.w)), bon1 = SUM16((z1.x + z1.y) + (z1.z + z1.w));
;                 if (c4 == 0) { LAS f32x4* cp = (LAS f32x4*)(buf + SC_C + pr * 20); cp[0] = ca; cp[1] = cb; cp[2] = cc; cp[3] = cd; cp[4] = (f32x4){ci, 0.f, 0.f, 0.f}; }
;                 buf[SC_BON + (2 * pr) * 8 + (c4 >> 1)] = bon0; buf[SC_BON + (2 * pr + 1) * 8 + (c4 >> 1)] = bon1;
	v_add_f32_dpp v2, v2, v2 quad_perm:[2,3,0,1] row_mask:0xf bank_mask:0xf bound_ctrl:1
	v_add_f32_dpp v3, v3, v3 quad_perm:[2,3,0,1] row_mask:0xf bank_mask:0xf bound_ctrl:1
	v_add_f32_dpp v4, v4, v4 quad_perm:[2,3,0,1] row_mask:0xf bank_mask:0xf bound_ctrl:1
	v_add_f32_dpp v5, v5, v5 quad_perm:[2,3,0,1] row_mask:0xf bank_mask:0xf bound_ctrl:1
	v_add_f32_dpp v22, v22, v22 quad_perm:[2,3,0,1] row_mask:0xf bank_mask:0xf bound_ctrl:1
	v_add_f32_dpp v23, v23, v23 quad_perm:[2,3,0,1] row_mask:0xf bank_mask:0xf bound_ctrl:1
	v_add_f32_dpp v24, v24, v24 quad_perm:[2,3,0,1] row_mask:0xf bank_mask:0xf bound_ctrl:1
	v_add_f32_dpp v25, v25, v25 quad_perm:[2,3,0,1] row_mask:0xf bank_mask:0xf bound_ctrl:1
	v_add_f32_dpp v26, v26, v26 quad_perm:[2,3,0,1] row_mask:0xf bank_mask:0xf bound_ctrl:1
	v_add_f32_dpp v6, v6, v6 quad_perm:[2,3,0,1] row_mask:0xf bank_mask:0xf bound_ctrl:1
	v_add_f32_dpp v7, v7, v7 quad_perm:[2,3,0,1] row_mask:0xf bank_mask:0xf bound_ctrl:1
	s_nop 1
	v_add_f32_dpp v10, v10, v10 row_half_mirror row_mask:0xf bank_mask:0xf bound_ctrl:1
	v_add_f32_dpp v11, v11, v11 row_half_mirror row_mask:0xf bank_mask:0xf bound_ctrl:1
	v_add_f32_dpp v12, v12, v12 row_half_mirror row_mask:0xf bank_mask:0xf bound_ctrl:1
	v_add_f32_dpp v13, v13, v13 row_half_mirror row_mask:0xf bank_mask:0xf bound_ctrl:1
	v_add_f32_dpp v14, v14, v14 row_half_mirror row_mask:0xf bank_mask:0xf bound_ctrl:1
	v_add_f32_dpp v15, v15, v15 row_half_mirror row_mask:0xf bank_mask:0xf bound_ctrl:1
	v_add_f32_dpp v16, v16, v16 row_half_mirror row_mask:0xf bank_mask:0xf bound_ctrl:1
	v_add_f32_dpp v17, v17, v17 row_half_mirror row_mask:0xf bank_mask:0xf bound_ctrl:1
	v_add_f32_dpp v2, v2, v2 row_half_mirror row_mask:0xf bank_mask:0xf bound_ctrl:1
	v_add_f32_dpp v3, v3, v3 row_half_mirror row_mask:0xf bank_mask:0xf bound_ctrl:1
	v_add_f32_dpp v4, v4, v4 row_half_mirror row_mask:0xf bank_mask:0xf bound_ctrl:1
	v_add_f32_dpp v5, v5, v5 row_half_mirror row_mask:0xf bank_mask:0xf bound_ctrl:1
	v_add_f32_dpp v22, v22, v22 row_half_mirror row_mask:0xf bank_mask:0xf bound_ctrl:1
	v_add_f32_dpp v23, v23, v23 row_half_mirror row_mask:0xf bank_mask:0xf bound_ctrl:1
	v_add_f32_dpp v24, v24, v24 row_half_mirror row_mask:0xf bank_mask:0xf bound_ctrl:1
	v_add_f32_dpp v25, v25, v25 row_half_mirror row_mask:0xf bank_mask:0xf bound_ctrl:1
	v_add_f32_dpp v26, v26, v26 row_half_mirror row_mask:0xf bank_mask:0xf bound_ctrl:1
	v_add_f32_dpp v6, v6, v6 row_half_mirror row_mask:0xf bank_mask:0xf bound_ctrl:1
	v_add_f32_dpp v7, v7, v7 row_half_mirror row_mask:0xf bank_mask:0xf bound_ctrl:1
	s_nop 1
	v_add_f32_dpp v10, v10, v10 row_mirror row_mask:0xf bank_mask:0xf bound_ctrl:1
	v_add_f32_dpp v11, v11, v11 row_mirror row_mask:0xf bank_mask:0xf bound_ctrl:1
	v_add_f32_dpp v12, v12, v12 row_mirror row_mask:0xf bank_mask:0xf bound_ctrl:1
	v_add_f32_dpp v13, v13, v13 row_mirror row_mask:0xf bank_mask:0xf bound_ctrl:1
	v_add_f32_dpp v14, v14, v14 row_mirror row_mask:0xf bank_mask:0xf bound_ctrl:1
	v_add_f32_dpp v15, v15, v15 row_mirror row_mask:0xf bank_mask:0xf bound_ctrl:1
	v_add_f32_dpp v16, v16, v16 row_mirror row_mask:0xf bank_mask:0xf bound_ctrl:1
	v_add_f32_dpp v17, v17, v17 row_mirror row_mask:0xf bank_mask:0xf bound_ctrl:1
	v_add_f32_dpp v2, v2, v2 row_mirror row_mask:0xf bank_mask:0xf bound_ctrl:1
	v_add_f32_dpp v3, v3, v3 row_mirror row_mask:0xf bank_mask:0xf bound_ctrl:1
	v_add_f32_dpp v4, v4, v4 row_mirror row_mask:0xf bank_mask:0xf bound_ctrl:1
	v_add_f32_dpp v5, v5, v5 row_mirror row_mask:0xf bank_mask:0xf bound_ctrl:1
	v_add_f32_dpp v22, v22, v22 row_mirror row_mask:0xf bank_mask:0xf bound_ctrl:1
	v_add_f32_dpp v23, v23, v23 row_mirror row_mask:0xf bank_mask:0xf bound_ctrl:1
	v_add_f32_dpp v24, v24, v24 row_mirror row_mask:0xf bank_mask:0xf bound_ctrl:1
	v_add_f32_dpp v25, v25, v25 row_mirror row_mask:0xf bank_mask:0xf bound_ctrl:1
	v_add_f32_dpp v26, v26, v26 row_mirror row_mask:0xf bank_mask:0xf bound_ctrl:1
	v_add_f32_dpp v6, v6, v6 row_mirror row_mask:0xf bank_mask:0xf bound_ctrl:1
	v_add_f32_dpp v7, v7, v7 row_mirror row_mask:0xf bank_mask:0xf bound_ctrl:1
	s_and_saveexec_b64 s[2:3], s[40:41]
	s_cbranch_execz .Lhb_1320
	v_add_u32_e32 v8, s1, v139
	v_mov_b32_e32 v27, v0
	v_mov_b32_e32 v28, v0
	v_mov_b32_e32 v29, v0
	ds_write_b128 v8, v[10:13] offset:36864
	ds_write_b128 v8, v[14:17] offset:36880
	ds_write_b128 v8, v[2:5] offset:36896
	ds_write_b128 v8, v[22:25] offset:36912
	ds_write_b128 v8, v[26:29] offset:36928
	s_branch .Lhb_1320
